# GEMM K-loops: removed the priority drop/raise pair that split each sub-phase's MFMA run
# baseline (speedup 1.0000x reference)
.LBB0_337:
	s_add_i32 s42, s19, s18
	s_mov_b32 m0, s42
	v_readfirstlane_b32 s6, v192
	v_readfirstlane_b32 s7, v193
	ds_read_b128 v[204:207], v203 offset:16384
	ds_read_b128 v[208:211], v203 offset:17408
	ds_read_b128 v[222:225], v203 offset:18432
	ds_read_b128 v[226:229], v203 offset:19456
	ds_read_b128 v[244:247], v203 offset:20480
	ds_read_b128 v[248:251], v203 offset:21504
	ds_read_b128 v[180:183], v203 offset:22528
	ds_read_b128 v[184:187], v203 offset:23552
	global_load_lds_dwordx4 v166, s[6:7]
	s_add_i32 m0, s42, 0x2000
	s_add_i32 s42, s20, s18
	global_load_lds_dwordx4 v170, s[6:7]
	s_mov_b32 m0, s42
	v_readfirstlane_b32 s6, v196
	v_readfirstlane_b32 s7, v197
	v_lshl_add_u64 v[198:199], v[200:201], 0, v[218:219]
	v_lshl_add_u64 v[200:201], v[200:201], 0, v[168:169]
	v_mov_b32_e32 v167, v219
	v_mov_b32_e32 v171, v219
	v_lshl_add_u64 v[190:191], v[192:193], 0, v[166:167]
	global_load_lds_dwordx4 v166, s[6:7]
	s_add_i32 m0, s42, 0x2000
	v_lshl_add_u64 v[192:193], v[192:193], 0, v[170:171]
	global_load_lds_dwordx4 v170, s[6:7]
	s_mov_b32 m0, s26
	v_lshl_add_u64 v[194:195], v[196:197], 0, v[166:167]
	global_load_lds_dwordx4 v[198:199], off
	s_add_i32 m0, s26, 0x2000
	v_lshl_add_u64 v[196:197], v[196:197], 0, v[170:171]
	global_load_lds_dwordx4 v[200:201], off
	s_waitcnt vmcnt(8)
	s_waitcnt lgkmcnt(0)
	s_barrier
	s_setprio 1
	s_waitcnt lgkmcnt(0)
	v_mfma_scale_f32_16x16x128_f8f6f4 v[94:97], v[18:25], v[204:211], v[94:97], v232, v232 op_sel_hi:[0,0,0]
	v_mfma_scale_f32_16x16x128_f8f6f4 v[90:93], v[26:33], v[204:211], v[90:93], v232, v232 op_sel_hi:[0,0,0]
	v_mfma_scale_f32_16x16x128_f8f6f4 v[78:81], v[18:25], v[222:229], v[78:81], v232, v232 op_sel_hi:[0,0,0]
	v_mfma_scale_f32_16x16x128_f8f6f4 v[74:77], v[26:33], v[222:229], v[74:77], v232, v232 op_sel_hi:[0,0,0]
	v_mfma_scale_f32_16x16x128_f8f6f4 v[62:65], v[18:25], v[244:251], v[62:65], v232, v232 op_sel_hi:[0,0,0]
	v_mfma_scale_f32_16x16x128_f8f6f4 v[58:61], v[26:33], v[244:251], v[58:61], v232, v232 op_sel_hi:[0,0,0]
	v_mfma_scale_f32_16x16x128_f8f6f4 v[46:49], v[18:25], v[180:187], v[46:49], v232, v232 op_sel_hi:[0,0,0]
	v_mfma_scale_f32_16x16x128_f8f6f4 v[42:45], v[26:33], v[180:187], v[42:45], v232, v232 op_sel_hi:[0,0,0]
	v_mfma_scale_f32_16x16x128_f8f6f4 v[86:89], v[2:9], v[204:211], v[86:89], v232, v232 op_sel_hi:[0,0,0]
	v_mfma_scale_f32_16x16x128_f8f6f4 v[82:85], v[10:17], v[204:211], v[82:85], v232, v232 op_sel_hi:[0,0,0]
	v_mfma_scale_f32_16x16x128_f8f6f4 v[70:73], v[2:9], v[222:229], v[70:73], v232, v232 op_sel_hi:[0,0,0]
	v_mfma_scale_f32_16x16x128_f8f6f4 v[66:69], v[10:17], v[222:229], v[66:69], v232, v232 op_sel_hi:[0,0,0]
	v_mfma_scale_f32_16x16x128_f8f6f4 v[54:57], v[2:9], v[244:251], v[54:57], v232, v232 op_sel_hi:[0,0,0]
	v_mfma_scale_f32_16x16x128_f8f6f4 v[50:53], v[10:17], v[244:251], v[50:53], v232, v232 op_sel_hi:[0,0,0]
	v_mfma_scale_f32_16x16x128_f8f6f4 v[38:41], v[2:9], v[180:187], v[38:41], v232, v232 op_sel_hi:[0,0,0]
	v_mfma_scale_f32_16x16x128_f8f6f4 v[34:37], v[10:17], v[180:187], v[34:37], v232, v232 op_sel_hi:[0,0,0]
	s_setprio 0
	s_barrier
	v_add_u32_e32 v14, s23, v202
	v_add_u32_e32 v30, s29, v202
	ds_read_b128 v[2:5], v14
	ds_read_b128 v[6:9], v14 offset:1024
	ds_read_b128 v[10:13], v14 offset:2048
	ds_read_b128 v[14:17], v14 offset:3072
	ds_read_b128 v[18:21], v30
	ds_read_b128 v[22:25], v30 offset:1024
	ds_read_b128 v[26:29], v30 offset:2048
	ds_read_b128 v[30:33], v30 offset:3072
	v_lshl_add_u64 v[240:241], v[188:189], 0, v[218:219]
	s_add_i32 m0, s26, 0x4000
	ds_read_b128 v[180:183], v203 offset:32768
	ds_read_b128 v[184:187], v203 offset:33792
	ds_read_b128 v[204:207], v203 offset:34816
	ds_read_b128 v[208:211], v203 offset:35840
	ds_read_b128 v[222:225], v203 offset:36864
	ds_read_b128 v[226:229], v203 offset:37888
	ds_read_b128 v[244:247], v203 offset:38912
	ds_read_b128 v[248:251], v203 offset:39936
	global_load_lds_dwordx4 v[240:241], off
	v_lshl_add_u64 v[188:189], v[188:189], 0, v[168:169]
	s_add_i32 m0, s26, 0x6000
	s_nop 0
	global_load_lds_dwordx4 v[188:189], off
	s_waitcnt vmcnt(8)
	s_waitcnt lgkmcnt(0)
	s_barrier
	s_setprio 1
	s_waitcnt lgkmcnt(0)
	v_mfma_scale_f32_16x16x128_f8f6f4 v[158:161], v[2:9], v[180:187], v[158:161], v232, v232 op_sel_hi:[0,0,0]
	v_mfma_scale_f32_16x16x128_f8f6f4 v[154:157], v[10:17], v[180:187], v[154:157], v232, v232 op_sel_hi:[0,0,0]
	v_mfma_scale_f32_16x16x128_f8f6f4 v[142:145], v[2:9], v[204:211], v[142:145], v232, v232 op_sel_hi:[0,0,0]
	v_mfma_scale_f32_16x16x128_f8f6f4 v[138:141], v[10:17], v[204:211], v[138:141], v232, v232 op_sel_hi:[0,0,0]
	v_mfma_scale_f32_16x16x128_f8f6f4 v[126:129], v[2:9], v[222:229], v[126:129], v232, v232 op_sel_hi:[0,0,0]
	v_mfma_scale_f32_16x16x128_f8f6f4 v[122:125], v[10:17], v[222:229], v[122:125], v232, v232 op_sel_hi:[0,0,0]
	v_mfma_scale_f32_16x16x128_f8f6f4 v[110:113], v[2:9], v[244:251], v[110:113], v232, v232 op_sel_hi:[0,0,0]
	v_mfma_scale_f32_16x16x128_f8f6f4 v[106:109], v[10:17], v[244:251], v[106:109], v232, v232 op_sel_hi:[0,0,0]
	v_mfma_scale_f32_16x16x128_f8f6f4 v[150:153], v[18:25], v[180:187], v[150:153], v232, v232 op_sel_hi:[0,0,0]
	v_mfma_scale_f32_16x16x128_f8f6f4 v[146:149], v[26:33], v[180:187], v[146:149], v232, v232 op_sel_hi:[0,0,0]
	v_mfma_scale_f32_16x16x128_f8f6f4 v[134:137], v[18:25], v[204:211], v[134:137], v232, v232 op_sel_hi:[0,0,0]
	v_mfma_scale_f32_16x16x128_f8f6f4 v[130:133], v[26:33], v[204:211], v[130:133], v232, v232 op_sel_hi:[0,0,0]
	v_mfma_scale_f32_16x16x128_f8f6f4 v[118:121], v[18:25], v[222:229], v[118:121], v232, v232 op_sel_hi:[0,0,0]
	v_mfma_scale_f32_16x16x128_f8f6f4 v[114:117], v[26:33], v[222:229], v[114:117], v232, v232 op_sel_hi:[0,0,0]
	v_mfma_scale_f32_16x16x128_f8f6f4 v[102:105], v[18:25], v[244:251], v[102:105], v232, v232 op_sel_hi:[0,0,0]
	v_mfma_scale_f32_16x16x128_f8f6f4 v[98:101], v[26:33], v[244:251], v[98:101], v232, v232 op_sel_hi:[0,0,0]
	s_setprio 0
	s_barrier
	s_mov_b32 m0, s24
	v_lshl_add_u64 v[188:189], v[190:191], 0, s[72:73]
	ds_read_b128 v[180:183], v203 offset:49152
	ds_read_b128 v[184:187], v203 offset:50176
	ds_read_b128 v[204:207], v203 offset:51200
	ds_read_b128 v[208:211], v203 offset:52224
	ds_read_b128 v[222:225], v203 offset:53248
	ds_read_b128 v[226:229], v203 offset:54272
	ds_read_b128 v[244:247], v203 offset:55296
	ds_read_b128 v[248:251], v203 offset:56320
	global_load_lds_dwordx4 v[188:189], off
	v_lshl_add_u64 v[188:189], v[192:193], 0, s[72:73]
	s_mov_b32 m0, s25
	s_nop 0
	global_load_lds_dwordx4 v[188:189], off
	v_lshl_add_u64 v[188:189], v[194:195], 0, s[72:73]
	s_mov_b32 m0, s30
	s_nop 0
	global_load_lds_dwordx4 v[188:189], off
	v_lshl_add_u64 v[188:189], v[196:197], 0, s[72:73]
	s_mov_b32 m0, s31
	s_nop 0
	global_load_lds_dwordx4 v[188:189], off
	v_lshl_add_u64 v[188:189], v[198:199], 0, s[72:73]
	s_mov_b32 m0, s27
	s_nop 0
	global_load_lds_dwordx4 v[188:189], off
	v_lshl_add_u64 v[188:189], v[200:201], 0, s[72:73]
	s_mov_b32 m0, s28
	s_nop 0
	global_load_lds_dwordx4 v[188:189], off
	s_waitcnt vmcnt(8)
	s_waitcnt lgkmcnt(0)
	s_barrier
	s_setprio 1
	s_waitcnt lgkmcnt(0)
	v_mfma_scale_f32_16x16x128_f8f6f4 v[94:97], v[2:9], v[180:187], v[94:97], v232, v232 op_sel_hi:[0,0,0]
	v_mfma_scale_f32_16x16x128_f8f6f4 v[90:93], v[10:17], v[180:187], v[90:93], v232, v232 op_sel_hi:[0,0,0]
	v_mfma_scale_f32_16x16x128_f8f6f4 v[78:81], v[2:9], v[204:211], v[78:81], v232, v232 op_sel_hi:[0,0,0]
	v_mfma_scale_f32_16x16x128_f8f6f4 v[74:77], v[10:17], v[204:211], v[74:77], v232, v232 op_sel_hi:[0,0,0]
	v_mfma_scale_f32_16x16x128_f8f6f4 v[62:65], v[2:9], v[222:229], v[62:65], v232, v232 op_sel_hi:[0,0,0]
	v_mfma_scale_f32_16x16x128_f8f6f4 v[58:61], v[10:17], v[222:229], v[58:61], v232, v232 op_sel_hi:[0,0,0]
	v_mfma_scale_f32_16x16x128_f8f6f4 v[46:49], v[2:9], v[244:251], v[46:49], v232, v232 op_sel_hi:[0,0,0]
	v_mfma_scale_f32_16x16x128_f8f6f4 v[42:45], v[10:17], v[244:251], v[42:45], v232, v232 op_sel_hi:[0,0,0]
	v_mfma_scale_f32_16x16x128_f8f6f4 v[86:89], v[18:25], v[180:187], v[86:89], v232, v232 op_sel_hi:[0,0,0]
	v_mfma_scale_f32_16x16x128_f8f6f4 v[82:85], v[26:33], v[180:187], v[82:85], v232, v232 op_sel_hi:[0,0,0]
	v_mfma_scale_f32_16x16x128_f8f6f4 v[70:73], v[18:25], v[204:211], v[70:73], v232, v232 op_sel_hi:[0,0,0]
	v_mfma_scale_f32_16x16x128_f8f6f4 v[66:69], v[26:33], v[204:211], v[66:69], v232, v232 op_sel_hi:[0,0,0]
	v_mfma_scale_f32_16x16x128_f8f6f4 v[54:57], v[18:25], v[222:229], v[54:57], v232, v232 op_sel_hi:[0,0,0]
	v_mfma_scale_f32_16x16x128_f8f6f4 v[50:53], v[26:33], v[222:229], v[50:53], v232, v232 op_sel_hi:[0,0,0]
	v_mfma_scale_f32_16x16x128_f8f6f4 v[38:41], v[18:25], v[244:251], v[38:41], v232, v232 op_sel_hi:[0,0,0]
	v_mfma_scale_f32_16x16x128_f8f6f4 v[34:37], v[26:33], v[244:251], v[34:37], v232, v232 op_sel_hi:[0,0,0]
	s_setprio 0
	s_barrier
	s_add_i32 s41, s41, 2
	s_add_u32 s14, s14, 0x100
	s_addc_u32 s15, s15, 0
	s_cmp_gt_u32 s41, 5
	s_cbranch_scc1 .LBB0_345
.LBB0_338:
	v_add_u32_e32 v2, s19, v202
	v_add_u32_e32 v14, s20, v202
	ds_read_b128 v[18:21], v2
	ds_read_b128 v[22:25], v2 offset:1024
	ds_read_b128 v[26:29], v2 offset:2048
	ds_read_b128 v[30:33], v2 offset:3072
	ds_read_b128 v[2:5], v14
	ds_read_b128 v[6:9], v14 offset:1024
	ds_read_b128 v[10:13], v14 offset:2048
	ds_read_b128 v[14:17], v14 offset:3072
	v_lshl_add_u64 v[188:189], v[176:177], 0, s[14:15]
	v_lshl_add_u64 v[180:181], v[188:189], 0, v[218:219]
	v_lshl_add_u64 v[180:181], v[180:181], 0, s[74:75]
	s_add_i32 m0, s26, 0xc000
	v_mov_b32_e32 v169, v219
	ds_read_b128 v[190:193], v203
	ds_read_b128 v[194:197], v203 offset:1024
	ds_read_b128 v[204:207], v203 offset:2048
	ds_read_b128 v[208:211], v203 offset:3072
	ds_read_b128 v[244:247], v203 offset:4096
	ds_read_b128 v[248:251], v203 offset:5120
	ds_read_b128 v[222:225], v203 offset:6144
	ds_read_b128 v[226:229], v203 offset:7168
	global_load_lds_dwordx4 v[180:181], off
	v_lshl_add_u64 v[180:181], v[188:189], 0, v[168:169]
	v_lshl_add_u64 v[180:181], v[180:181], 0, s[74:75]
	s_add_i32 m0, s26, 0xe000
	s_nop 0
	global_load_lds_dwordx4 v[180:181], off
	s_waitcnt vmcnt(8)
	s_waitcnt lgkmcnt(0)
	s_barrier
	s_setprio 1
	s_waitcnt lgkmcnt(0)
	v_mfma_scale_f32_16x16x128_f8f6f4 v[158:161], v[18:25], v[190:197], v[158:161], v232, v232 op_sel_hi:[0,0,0]
	v_mfma_scale_f32_16x16x128_f8f6f4 v[154:157], v[26:33], v[190:197], v[154:157], v232, v232 op_sel_hi:[0,0,0]
	v_mfma_scale_f32_16x16x128_f8f6f4 v[142:145], v[18:25], v[204:211], v[142:145], v232, v232 op_sel_hi:[0,0,0]
	v_mfma_scale_f32_16x16x128_f8f6f4 v[138:141], v[26:33], v[204:211], v[138:141], v232, v232 op_sel_hi:[0,0,0]
	v_mfma_scale_f32_16x16x128_f8f6f4 v[126:129], v[18:25], v[244:251], v[126:129], v232, v232 op_sel_hi:[0,0,0]
	v_mfma_scale_f32_16x16x128_f8f6f4 v[122:125], v[26:33], v[244:251], v[122:125], v232, v232 op_sel_hi:[0,0,0]
	v_mfma_scale_f32_16x16x128_f8f6f4 v[110:113], v[18:25], v[222:229], v[110:113], v232, v232 op_sel_hi:[0,0,0]
	v_mfma_scale_f32_16x16x128_f8f6f4 v[106:109], v[26:33], v[222:229], v[106:109], v232, v232 op_sel_hi:[0,0,0]
	v_mfma_scale_f32_16x16x128_f8f6f4 v[150:153], v[2:9], v[190:197], v[150:153], v232, v232 op_sel_hi:[0,0,0]
	v_mfma_scale_f32_16x16x128_f8f6f4 v[146:149], v[10:17], v[190:197], v[146:149], v232, v232 op_sel_hi:[0,0,0]
	v_mfma_scale_f32_16x16x128_f8f6f4 v[134:137], v[2:9], v[204:211], v[134:137], v232, v232 op_sel_hi:[0,0,0]
	v_mfma_scale_f32_16x16x128_f8f6f4 v[130:133], v[10:17], v[204:211], v[130:133], v232, v232 op_sel_hi:[0,0,0]
	v_mfma_scale_f32_16x16x128_f8f6f4 v[118:121], v[2:9], v[244:251], v[118:121], v232, v232 op_sel_hi:[0,0,0]
	v_mfma_scale_f32_16x16x128_f8f6f4 v[114:117], v[10:17], v[244:251], v[114:117], v232, v232 op_sel_hi:[0,0,0]
	v_mfma_scale_f32_16x16x128_f8f6f4 v[102:105], v[2:9], v[222:229], v[102:105], v232, v232 op_sel_hi:[0,0,0]
	v_mfma_scale_f32_16x16x128_f8f6f4 v[98:101], v[10:17], v[222:229], v[98:101], v232, v232 op_sel_hi:[0,0,0]
	s_cmpk_lg_i32 s14, 0x300
	s_setprio 0
	s_barrier
	s_cbranch_scc0 .LBB0_340
	s_mov_b64 s[6:7], 0x20100
	v_lshl_add_u64 v[200:201], v[188:189], 0, s[76:77]
	v_lshl_add_u64 v[180:181], v[178:179], 0, s[14:15]
	v_lshl_add_u64 v[188:189], v[188:189], 0, s[6:7]
	s_mov_b64 s[6:7], 0x8100
	v_lshl_add_u64 v[192:193], v[180:181], 0, s[76:77]
	v_lshl_add_u64 v[196:197], v[180:181], 0, s[6:7]
	s_cbranch_execnz .LBB0_337
	s_branch .LBB0_341

.LBB0_543:
	v_add_u32_e32 v2, s15, v174
	v_add_u32_e32 v22, s16, v174
	ds_read_b128 v[10:13], v2
	ds_read_b128 v[14:17], v2 offset:1024
	ds_read_b128 v[26:29], v2 offset:2048
	ds_read_b128 v[30:33], v2 offset:3072
	ds_read_b128 v[2:5], v22
	ds_read_b128 v[6:9], v22 offset:1024
	ds_read_b128 v[18:21], v22 offset:2048
	ds_read_b128 v[22:25], v22 offset:3072
	s_mov_b64 s[4:5], 0x10080
	v_lshl_add_u64 v[34:35], v[164:165], 0, s[4:5]
	s_add_i32 m0, s20, 0xc000
	v_readfirstlane_b32 s4, v34
	v_readfirstlane_b32 s5, v35
	ds_read_b128 v[62:65], v175
	ds_read_b128 v[66:69], v175 offset:1024
	ds_read_b128 v[90:93], v175 offset:2048
	ds_read_b128 v[94:97], v175 offset:3072
	ds_read_b128 v[114:117], v175 offset:4096
	ds_read_b128 v[118:121], v175 offset:5120
	ds_read_b128 v[122:125], v175 offset:6144
	ds_read_b128 v[126:129], v175 offset:7168
	global_load_lds_dwordx4 v218, s[4:5]
	s_add_i32 m0, s20, 0xe000
	s_nop 0
	global_load_lds_dwordx4 v154, s[4:5]
	s_waitcnt vmcnt(8)
	s_waitcnt lgkmcnt(0)
	s_barrier
	s_setprio 1
	v_mov_b64_e32 v[34:35], s[88:89]
	v_mov_b64_e32 v[104:105], s[90:91]
	v_mov_b64_e32 v[100:101], s[90:91]
	v_mov_b64_e32 v[78:79], s[88:89]
	v_mov_b64_e32 v[74:75], s[88:89]
	v_mov_b64_e32 v[58:59], s[88:89]
	v_mov_b64_e32 v[50:51], s[88:89]
	v_mov_b64_e32 v[42:43], s[88:89]
	v_mov_b64_e32 v[38:39], s[88:89]
	v_mov_b64_e32 v[36:37], s[90:91]
	v_mov_b64_e32 v[102:103], s[88:89]
	v_mov_b64_e32 v[98:99], s[88:89]
	v_mov_b64_e32 v[80:81], s[90:91]
	v_mov_b64_e32 v[76:77], s[90:91]
	v_mov_b64_e32 v[60:61], s[90:91]
	v_mov_b64_e32 v[52:53], s[90:91]
	v_mov_b64_e32 v[44:45], s[90:91]
	v_mov_b64_e32 v[40:41], s[90:91]
	s_waitcnt lgkmcnt(0)
	v_mfma_scale_f32_16x16x128_f8f6f4 v[102:105], v[10:17], v[62:69], v[102:105], v232, v232 op_sel_hi:[0,0,0]
	v_mfma_scale_f32_16x16x128_f8f6f4 v[98:101], v[26:33], v[62:69], v[98:101], v232, v232 op_sel_hi:[0,0,0]
	v_mfma_scale_f32_16x16x128_f8f6f4 v[78:81], v[10:17], v[90:97], v[78:81], v232, v232 op_sel_hi:[0,0,0]
	v_mfma_scale_f32_16x16x128_f8f6f4 v[74:77], v[26:33], v[90:97], v[74:77], v232, v232 op_sel_hi:[0,0,0]
	v_mfma_scale_f32_16x16x128_f8f6f4 v[58:61], v[10:17], v[114:121], v[58:61], v232, v232 op_sel_hi:[0,0,0]
	v_mfma_scale_f32_16x16x128_f8f6f4 v[50:53], v[26:33], v[114:121], v[50:53], v232, v232 op_sel_hi:[0,0,0]
	v_mfma_scale_f32_16x16x128_f8f6f4 v[42:45], v[10:17], v[122:129], v[42:45], v232, v232 op_sel_hi:[0,0,0]
	v_mfma_scale_f32_16x16x128_f8f6f4 v[38:41], v[26:33], v[122:129], v[38:41], v232, v232 op_sel_hi:[0,0,0]
	v_mov_b64_e32 v[112:113], s[90:91]
	v_mov_b64_e32 v[108:109], s[90:91]
	v_mov_b64_e32 v[110:111], s[88:89]
	v_mov_b64_e32 v[106:107], s[88:89]
	v_mfma_scale_f32_16x16x128_f8f6f4 v[110:113], v[2:9], v[62:69], v[110:113], v232, v232 op_sel_hi:[0,0,0]
	v_mfma_scale_f32_16x16x128_f8f6f4 v[106:109], v[18:25], v[62:69], v[106:109], v232, v232 op_sel_hi:[0,0,0]
	v_mov_b64_e32 v[86:87], s[88:89]
	v_mov_b64_e32 v[82:83], s[88:89]
	v_mov_b64_e32 v[62:63], s[88:89]
	v_mov_b64_e32 v[54:55], s[88:89]
	v_mov_b64_e32 v[46:47], s[88:89]
	v_mov_b64_e32 v[88:89], s[90:91]
	v_mov_b64_e32 v[84:85], s[90:91]
	v_mov_b64_e32 v[64:65], s[90:91]
	v_mov_b64_e32 v[56:57], s[90:91]
	v_mov_b64_e32 v[48:49], s[90:91]
	v_mfma_scale_f32_16x16x128_f8f6f4 v[86:89], v[2:9], v[90:97], v[86:89], v232, v232 op_sel_hi:[0,0,0]
	v_mfma_scale_f32_16x16x128_f8f6f4 v[82:85], v[18:25], v[90:97], v[82:85], v232, v232 op_sel_hi:[0,0,0]
	v_mfma_scale_f32_16x16x128_f8f6f4 v[62:65], v[2:9], v[114:121], v[62:65], v232, v232 op_sel_hi:[0,0,0]
	v_mfma_scale_f32_16x16x128_f8f6f4 v[54:57], v[18:25], v[114:121], v[54:57], v232, v232 op_sel_hi:[0,0,0]
	v_mfma_scale_f32_16x16x128_f8f6f4 v[46:49], v[2:9], v[122:129], v[46:49], v232, v232 op_sel_hi:[0,0,0]
	v_mfma_scale_f32_16x16x128_f8f6f4 v[34:37], v[18:25], v[122:129], v[34:37], v232, v232 op_sel_hi:[0,0,0]
	s_setprio 0
	s_barrier
	v_mov_b64_e32 v[66:67], 0x1ce
	v_cmp_lt_i64_e64 s[6:7], s[12:13], v[66:67]
	v_mov_b64_e32 v[66:67], 0x1cd
	v_cmp_gt_i64_e32 vcc, s[12:13], v[66:67]
	s_cbranch_vccnz .LBB0_549
	s_ashr_i32 s4, s12, 31
	s_lshr_b32 s4, s4, 29
	s_add_i32 s28, s12, s4
	s_and_b32 s4, s28, -8
	s_sub_i32 s29, s12, s4
	s_cmp_gt_i32 s29, 5
	s_mov_b64 s[4:5], -1
	s_cbranch_scc0 .LBB0_546
	s_mul_i32 s4, s29, 57
	s_add_i32 s33, s4, 6
	s_mov_b64 s[4:5], 0

.LBB0_551:
	s_mov_b64 s[6:7], 0x2000
	s_add_i32 s33, s15, s14
	v_lshl_add_u64 v[66:67], v[162:163], 0, s[6:7]
	s_mov_b32 m0, s33
	v_readfirstlane_b32 s6, v162
	v_readfirstlane_b32 s7, v163
	ds_read_b128 v[122:125], v175 offset:16384
	ds_read_b128 v[126:129], v175 offset:17408
	ds_read_b128 v[176:179], v175 offset:18432
	ds_read_b128 v[180:183], v175 offset:19456
	ds_read_b128 v[184:187], v175 offset:20480
	ds_read_b128 v[188:191], v175 offset:21504
	ds_read_b128 v[192:195], v175 offset:22528
	ds_read_b128 v[196:199], v175 offset:23552
	global_load_lds_dwordx4 v152, s[6:7]
	s_add_i32 m0, s33, 0x2000
	s_add_i32 s33, s16, s14
	global_load_lds_dwordx4 v156, s[6:7]
	s_mov_b32 m0, s33
	v_readfirstlane_b32 s6, v66
	v_readfirstlane_b32 s7, v67
	v_lshl_add_u64 v[170:171], v[164:165], 0, v[218:219]
	v_lshl_add_u64 v[172:173], v[164:165], 0, v[154:155]
	v_mov_b32_e32 v153, v219
	v_mov_b32_e32 v157, v219
	v_lshl_add_u64 v[166:167], v[162:163], 0, v[152:153]
	global_load_lds_dwordx4 v152, s[6:7]
	s_add_i32 m0, s33, 0x2000
	v_lshl_add_u64 v[168:169], v[162:163], 0, v[156:157]
	global_load_lds_dwordx4 v156, s[6:7]
	s_mov_b32 m0, s20
	s_nop 0
	global_load_lds_dwordx4 v[170:171], off
	s_add_i32 m0, s20, 0x2000
	s_nop 0
	global_load_lds_dwordx4 v[172:173], off
	s_waitcnt vmcnt(8)
	s_waitcnt lgkmcnt(0)
	s_barrier
	s_setprio 1
	v_mov_b64_e32 v[136:137], s[90:91]
	v_mov_b64_e32 v[132:133], s[90:91]
	v_mov_b64_e32 v[120:121], s[90:91]
	v_mov_b64_e32 v[116:117], s[90:91]
	v_mov_b64_e32 v[96:97], s[90:91]
	v_mov_b64_e32 v[92:93], s[90:91]
	v_mov_b64_e32 v[70:71], s[88:89]
	v_mov_b64_e32 v[134:135], s[88:89]
	v_mov_b64_e32 v[130:131], s[88:89]
	v_mov_b64_e32 v[118:119], s[88:89]
	v_mov_b64_e32 v[114:115], s[88:89]
	v_mov_b64_e32 v[94:95], s[88:89]
	v_mov_b64_e32 v[90:91], s[88:89]
	v_mov_b64_e32 v[72:73], s[90:91]
	v_mov_b64_e32 v[66:67], s[88:89]
	s_waitcnt lgkmcnt(0)
	v_mfma_scale_f32_16x16x128_f8f6f4 v[134:137], v[10:17], v[122:129], v[134:137], v232, v232 op_sel_hi:[0,0,0]
	v_mfma_scale_f32_16x16x128_f8f6f4 v[130:133], v[26:33], v[122:129], v[130:133], v232, v232 op_sel_hi:[0,0,0]
	v_mfma_scale_f32_16x16x128_f8f6f4 v[118:121], v[10:17], v[176:183], v[118:121], v232, v232 op_sel_hi:[0,0,0]
	v_mfma_scale_f32_16x16x128_f8f6f4 v[114:117], v[26:33], v[176:183], v[114:117], v232, v232 op_sel_hi:[0,0,0]
	v_mfma_scale_f32_16x16x128_f8f6f4 v[94:97], v[10:17], v[184:191], v[94:97], v232, v232 op_sel_hi:[0,0,0]
	v_mfma_scale_f32_16x16x128_f8f6f4 v[90:93], v[26:33], v[184:191], v[90:93], v232, v232 op_sel_hi:[0,0,0]
	v_mfma_scale_f32_16x16x128_f8f6f4 v[70:73], v[10:17], v[192:199], v[70:73], v232, v232 op_sel_hi:[0,0,0]
	v_mov_b64_e32 v[10:11], s[88:89]
	v_mov_b64_e32 v[68:69], s[90:91]
	v_mov_b64_e32 v[12:13], s[90:91]
	v_mfma_scale_f32_16x16x128_f8f6f4 v[10:13], v[26:33], v[192:199], v[10:13], v232, v232 op_sel_hi:[0,0,0]
	v_mov_b64_e32 v[144:145], s[90:91]
	v_mov_b64_e32 v[140:141], s[90:91]
	v_mov_b64_e32 v[142:143], s[88:89]
	v_mov_b64_e32 v[138:139], s[88:89]
	v_mfma_scale_f32_16x16x128_f8f6f4 v[142:145], v[2:9], v[122:129], v[142:145], v232, v232 op_sel_hi:[0,0,0]
	v_mfma_scale_f32_16x16x128_f8f6f4 v[138:141], v[18:25], v[122:129], v[138:141], v232, v232 op_sel_hi:[0,0,0]
	v_mov_b64_e32 v[128:129], s[90:91]
	v_mov_b64_e32 v[124:125], s[90:91]
	v_mov_b64_e32 v[30:31], s[88:89]
	v_mov_b64_e32 v[26:27], s[88:89]
	v_mov_b64_e32 v[14:15], s[88:89]
	v_mov_b64_e32 v[126:127], s[88:89]
	v_mov_b64_e32 v[122:123], s[88:89]
	v_mov_b64_e32 v[32:33], s[90:91]
	v_mov_b64_e32 v[28:29], s[90:91]
	v_mov_b64_e32 v[16:17], s[90:91]
	v_mfma_scale_f32_16x16x128_f8f6f4 v[126:129], v[2:9], v[176:183], v[126:129], v232, v232 op_sel_hi:[0,0,0]
	v_mfma_scale_f32_16x16x128_f8f6f4 v[122:125], v[18:25], v[176:183], v[122:125], v232, v232 op_sel_hi:[0,0,0]
	v_mfma_scale_f32_16x16x128_f8f6f4 v[30:33], v[2:9], v[184:191], v[30:33], v232, v232 op_sel_hi:[0,0,0]
	v_mfma_scale_f32_16x16x128_f8f6f4 v[26:29], v[18:25], v[184:191], v[26:29], v232, v232 op_sel_hi:[0,0,0]
	v_mfma_scale_f32_16x16x128_f8f6f4 v[14:17], v[2:9], v[192:199], v[14:17], v232, v232 op_sel_hi:[0,0,0]
	v_mfma_scale_f32_16x16x128_f8f6f4 v[66:69], v[18:25], v[192:199], v[66:69], v232, v232 op_sel_hi:[0,0,0]
	s_setprio 0
	s_barrier
	v_add_u32_e32 v22, s17, v174
	v_add_u32_e32 v153, s23, v174
	ds_read_b128 v[2:5], v22
	ds_read_b128 v[6:9], v22 offset:1024
	ds_read_b128 v[18:21], v22 offset:2048
	ds_read_b128 v[22:25], v22 offset:3072
	ds_read_b128 v[176:179], v153
	ds_read_b128 v[180:183], v153 offset:1024
	ds_read_b128 v[184:187], v153 offset:2048
	ds_read_b128 v[188:191], v153 offset:3072
	v_lshl_add_u64 v[164:165], v[164:165], 0, s[60:61]
	v_lshl_add_u64 v[216:217], v[164:165], 0, v[218:219]
	s_add_i32 m0, s20, 0x4000
	ds_read_b128 v[192:195], v175 offset:32768
	ds_read_b128 v[196:199], v175 offset:33792
	ds_read_b128 v[200:203], v175 offset:34816
	ds_read_b128 v[204:207], v175 offset:35840
	ds_read_b128 v[208:211], v175 offset:36864
	ds_read_b128 v[212:215], v175 offset:37888
	ds_read_b128 v[222:225], v175 offset:38912
	ds_read_b128 v[226:229], v175 offset:39936
	global_load_lds_dwordx4 v[216:217], off
	v_lshl_add_u64 v[164:165], v[164:165], 0, v[154:155]
	s_add_i32 m0, s20, 0x6000
	s_nop 0
	global_load_lds_dwordx4 v[164:165], off
	s_waitcnt vmcnt(8)
	s_waitcnt lgkmcnt(0)
	s_barrier
	s_setprio 1
	s_waitcnt lgkmcnt(0)
	v_mfma_scale_f32_16x16x128_f8f6f4 v[102:105], v[2:9], v[192:199], v[102:105], v232, v232 op_sel_hi:[0,0,0]
	v_mfma_scale_f32_16x16x128_f8f6f4 v[98:101], v[18:25], v[192:199], v[98:101], v232, v232 op_sel_hi:[0,0,0]
	v_mfma_scale_f32_16x16x128_f8f6f4 v[78:81], v[2:9], v[200:207], v[78:81], v232, v232 op_sel_hi:[0,0,0]
	v_mfma_scale_f32_16x16x128_f8f6f4 v[74:77], v[18:25], v[200:207], v[74:77], v232, v232 op_sel_hi:[0,0,0]
	v_mfma_scale_f32_16x16x128_f8f6f4 v[58:61], v[2:9], v[208:215], v[58:61], v232, v232 op_sel_hi:[0,0,0]
	v_mfma_scale_f32_16x16x128_f8f6f4 v[50:53], v[18:25], v[208:215], v[50:53], v232, v232 op_sel_hi:[0,0,0]
	v_mfma_scale_f32_16x16x128_f8f6f4 v[42:45], v[2:9], v[222:229], v[42:45], v232, v232 op_sel_hi:[0,0,0]
	v_mfma_scale_f32_16x16x128_f8f6f4 v[38:41], v[18:25], v[222:229], v[38:41], v232, v232 op_sel_hi:[0,0,0]
	v_mfma_scale_f32_16x16x128_f8f6f4 v[110:113], v[176:183], v[192:199], v[110:113], v232, v232 op_sel_hi:[0,0,0]
	v_mfma_scale_f32_16x16x128_f8f6f4 v[106:109], v[184:191], v[192:199], v[106:109], v232, v232 op_sel_hi:[0,0,0]
	v_mfma_scale_f32_16x16x128_f8f6f4 v[86:89], v[176:183], v[200:207], v[86:89], v232, v232 op_sel_hi:[0,0,0]
	v_mfma_scale_f32_16x16x128_f8f6f4 v[82:85], v[184:191], v[200:207], v[82:85], v232, v232 op_sel_hi:[0,0,0]
	v_mfma_scale_f32_16x16x128_f8f6f4 v[62:65], v[176:183], v[208:215], v[62:65], v232, v232 op_sel_hi:[0,0,0]
	v_mfma_scale_f32_16x16x128_f8f6f4 v[54:57], v[184:191], v[208:215], v[54:57], v232, v232 op_sel_hi:[0,0,0]
	v_mfma_scale_f32_16x16x128_f8f6f4 v[46:49], v[176:183], v[222:229], v[46:49], v232, v232 op_sel_hi:[0,0,0]
	v_mfma_scale_f32_16x16x128_f8f6f4 v[34:37], v[184:191], v[222:229], v[34:37], v232, v232 op_sel_hi:[0,0,0]
	s_setprio 0
	s_barrier
	s_mov_b32 m0, s18
	v_lshl_add_u64 v[164:165], v[166:167], 0, s[72:73]
	s_mov_b64 s[6:7], 0x2080
	ds_read_b128 v[192:195], v175 offset:49152
	ds_read_b128 v[196:199], v175 offset:50176
	ds_read_b128 v[200:203], v175 offset:51200
	ds_read_b128 v[204:207], v175 offset:52224
	ds_read_b128 v[208:211], v175 offset:53248
	ds_read_b128 v[212:215], v175 offset:54272
	ds_read_b128 v[222:225], v175 offset:55296
	ds_read_b128 v[226:229], v175 offset:56320
	global_load_lds_dwordx4 v[164:165], off
	v_lshl_add_u64 v[164:165], v[168:169], 0, s[72:73]
	s_mov_b32 m0, s19
	v_lshl_add_u64 v[162:163], v[162:163], 0, s[6:7]
	global_load_lds_dwordx4 v[164:165], off
	v_readfirstlane_b32 s6, v162
	v_readfirstlane_b32 s7, v163
	s_mov_b32 m0, s24
	v_lshl_add_u64 v[162:163], v[170:171], 0, s[72:73]
	s_nop 2
	global_load_lds_dwordx4 v152, s[6:7]
	s_mov_b32 m0, s25
	s_nop 0
	global_load_lds_dwordx4 v156, s[6:7]
	s_mov_b32 m0, s21
	s_nop 0
	global_load_lds_dwordx4 v[162:163], off
	v_lshl_add_u64 v[162:163], v[172:173], 0, s[72:73]
	s_mov_b32 m0, s22
	s_nop 0
	global_load_lds_dwordx4 v[162:163], off
	s_waitcnt vmcnt(8)
	s_waitcnt lgkmcnt(0)
	s_barrier
	s_setprio 1
	s_waitcnt lgkmcnt(0)
	v_mfma_scale_f32_16x16x128_f8f6f4 v[134:137], v[2:9], v[192:199], v[134:137], v232, v232 op_sel_hi:[0,0,0]
	v_mfma_scale_f32_16x16x128_f8f6f4 v[130:133], v[18:25], v[192:199], v[130:133], v232, v232 op_sel_hi:[0,0,0]
	v_mfma_scale_f32_16x16x128_f8f6f4 v[118:121], v[2:9], v[200:207], v[118:121], v232, v232 op_sel_hi:[0,0,0]
	v_mfma_scale_f32_16x16x128_f8f6f4 v[114:117], v[18:25], v[200:207], v[114:117], v232, v232 op_sel_hi:[0,0,0]
	v_mfma_scale_f32_16x16x128_f8f6f4 v[94:97], v[2:9], v[208:215], v[94:97], v232, v232 op_sel_hi:[0,0,0]
	v_mfma_scale_f32_16x16x128_f8f6f4 v[90:93], v[18:25], v[208:215], v[90:93], v232, v232 op_sel_hi:[0,0,0]
	v_mfma_scale_f32_16x16x128_f8f6f4 v[70:73], v[2:9], v[222:229], v[70:73], v232, v232 op_sel_hi:[0,0,0]
	v_mfma_scale_f32_16x16x128_f8f6f4 v[10:13], v[18:25], v[222:229], v[10:13], v232, v232 op_sel_hi:[0,0,0]
	v_mfma_scale_f32_16x16x128_f8f6f4 v[142:145], v[176:183], v[192:199], v[142:145], v232, v232 op_sel_hi:[0,0,0]
	v_mfma_scale_f32_16x16x128_f8f6f4 v[138:141], v[184:191], v[192:199], v[138:141], v232, v232 op_sel_hi:[0,0,0]
	v_mfma_scale_f32_16x16x128_f8f6f4 v[126:129], v[176:183], v[200:207], v[126:129], v232, v232 op_sel_hi:[0,0,0]
	v_mfma_scale_f32_16x16x128_f8f6f4 v[122:125], v[184:191], v[200:207], v[122:125], v232, v232 op_sel_hi:[0,0,0]
	v_mfma_scale_f32_16x16x128_f8f6f4 v[30:33], v[176:183], v[208:215], v[30:33], v232, v232 op_sel_hi:[0,0,0]
	v_mfma_scale_f32_16x16x128_f8f6f4 v[26:29], v[184:191], v[208:215], v[26:29], v232, v232 op_sel_hi:[0,0,0]
	v_mfma_scale_f32_16x16x128_f8f6f4 v[14:17], v[176:183], v[222:229], v[14:17], v232, v232 op_sel_hi:[0,0,0]
	v_mfma_scale_f32_16x16x128_f8f6f4 v[66:69], v[184:191], v[222:229], v[66:69], v232, v232 op_sel_hi:[0,0,0]
	s_setprio 0
	s_barrier
	s_andn2_b64 vcc, exec, s[10:11]
	s_cbranch_vccnz .LBB0_553
	s_barrier

.LBB0_1008:
	s_mov_b32 m0, s45
	ds_read_b128 v[174:177], v173 offset:16384
	ds_read_b128 v[178:181], v173 offset:17408
	ds_read_b128 v[182:185], v173 offset:18432
	ds_read_b128 v[186:189], v173 offset:19456
	ds_read_b128 v[190:193], v173 offset:20480
	ds_read_b128 v[194:197], v173 offset:21504
	ds_read_b128 v[198:201], v173 offset:22528
	ds_read_b128 v[202:205], v173 offset:23552
	global_load_lds_dwordx4 v164, s[60:61]
	s_mov_b32 m0, s46
	v_lshl_add_u64 v[212:213], s[34:35], 0, v[218:219]
	global_load_lds_dwordx4 v168, s[60:61]
	s_mov_b32 m0, s48
	v_lshl_add_u64 v[214:215], s[34:35], 0, v[166:167]
	global_load_lds_dwordx4 v164, s[56:57]
	s_mov_b32 m0, s49
	v_mov_b32_e32 v165, v219
	global_load_lds_dwordx4 v168, s[56:57]
	s_mov_b32 m0, s50
	v_mov_b32_e32 v169, v219
	global_load_lds_dwordx4 v[212:213], off
	s_mov_b32 m0, s51
	v_lshl_add_u64 v[170:171], s[60:61], 0, v[164:165]
	global_load_lds_dwordx4 v[214:215], off
	s_waitcnt vmcnt(8)
	s_waitcnt lgkmcnt(0)
	v_lshl_add_u64 v[206:207], s[60:61], 0, v[168:169]
	v_lshl_add_u64 v[208:209], s[56:57], 0, v[164:165]
	v_lshl_add_u64 v[210:211], s[56:57], 0, v[168:169]
	s_barrier
	s_setprio 1
	s_waitcnt lgkmcnt(0)
	v_mfma_f32_16x16x32_bf16 v[62:65], v[146:149], v[174:177], v[62:65]
	v_mfma_f32_16x16x32_bf16 v[58:61], v[154:157], v[174:177], v[58:61]
	v_mfma_f32_16x16x32_bf16 v[54:57], v[146:149], v[182:185], v[54:57]
	v_mfma_f32_16x16x32_bf16 v[50:53], v[154:157], v[182:185], v[50:53]
	v_mfma_f32_16x16x32_bf16 v[46:49], v[146:149], v[190:193], v[46:49]
	v_mfma_f32_16x16x32_bf16 v[42:45], v[154:157], v[190:193], v[42:45]
	v_mfma_f32_16x16x32_bf16 v[38:41], v[146:149], v[198:201], v[38:41]
	v_mfma_f32_16x16x32_bf16 v[34:37], v[154:157], v[198:201], v[34:37]
	v_mfma_f32_16x16x32_bf16 v[62:65], v[150:153], v[178:181], v[62:65]
	v_mfma_f32_16x16x32_bf16 v[58:61], v[158:161], v[178:181], v[58:61]
	v_mfma_f32_16x16x32_bf16 v[54:57], v[150:153], v[186:189], v[54:57]
	v_mfma_f32_16x16x32_bf16 v[50:53], v[158:161], v[186:189], v[50:53]
	v_mfma_f32_16x16x32_bf16 v[46:49], v[150:153], v[194:197], v[46:49]
	v_mfma_f32_16x16x32_bf16 v[42:45], v[158:161], v[194:197], v[42:45]
	v_mfma_f32_16x16x32_bf16 v[38:41], v[150:153], v[202:205], v[38:41]
	v_mfma_f32_16x16x32_bf16 v[34:37], v[158:161], v[202:205], v[34:37]
	v_mfma_f32_16x16x32_bf16 v[30:33], v[130:133], v[174:177], v[30:33]
	v_mfma_f32_16x16x32_bf16 v[26:29], v[138:141], v[174:177], v[26:29]
	v_mfma_f32_16x16x32_bf16 v[22:25], v[130:133], v[182:185], v[22:25]
	v_mfma_f32_16x16x32_bf16 v[18:21], v[138:141], v[182:185], v[18:21]
	v_mfma_f32_16x16x32_bf16 v[14:17], v[130:133], v[190:193], v[14:17]
	v_mfma_f32_16x16x32_bf16 v[10:13], v[138:141], v[190:193], v[10:13]
	v_mfma_f32_16x16x32_bf16 v[6:9], v[130:133], v[198:201], v[6:9]
	v_mfma_f32_16x16x32_bf16 v[2:5], v[138:141], v[198:201], v[2:5]
	v_mfma_f32_16x16x32_bf16 v[30:33], v[134:137], v[178:181], v[30:33]
	v_mfma_f32_16x16x32_bf16 v[26:29], v[142:145], v[178:181], v[26:29]
	v_mfma_f32_16x16x32_bf16 v[22:25], v[134:137], v[186:189], v[22:25]
	v_mfma_f32_16x16x32_bf16 v[18:21], v[142:145], v[186:189], v[18:21]
	v_mfma_f32_16x16x32_bf16 v[14:17], v[134:137], v[194:197], v[14:17]
	v_mfma_f32_16x16x32_bf16 v[10:13], v[142:145], v[194:197], v[10:13]
	v_mfma_f32_16x16x32_bf16 v[6:9], v[134:137], v[202:205], v[6:9]
	v_mfma_f32_16x16x32_bf16 v[2:5], v[142:145], v[202:205], v[2:5]
	s_setprio 0
	s_barrier
	v_add_u32_e32 v142, s58, v172
	v_add_u32_e32 v158, s80, v172
	ds_read_b128 v[130:133], v142
	ds_read_b128 v[134:137], v142 offset:1024
	ds_read_b128 v[138:141], v142 offset:2048
	ds_read_b128 v[142:145], v142 offset:3072
	ds_read_b128 v[146:149], v158
	ds_read_b128 v[150:153], v158 offset:1024
	ds_read_b128 v[154:157], v158 offset:2048
	ds_read_b128 v[158:161], v158 offset:3072
	s_mov_b32 m0, s52
	v_lshl_add_u64 v[216:217], s[6:7], 0, v[218:219]
	ds_read_b128 v[174:177], v173 offset:32768
	ds_read_b128 v[178:181], v173 offset:33792
	ds_read_b128 v[182:185], v173 offset:34816
	ds_read_b128 v[186:189], v173 offset:35840
	ds_read_b128 v[190:193], v173 offset:36864
	ds_read_b128 v[194:197], v173 offset:37888
	ds_read_b128 v[198:201], v173 offset:38912
	ds_read_b128 v[202:205], v173 offset:39936
	global_load_lds_dwordx4 v[216:217], off
	v_lshl_add_u64 v[216:217], s[6:7], 0, v[166:167]
	s_mov_b32 m0, s53
	s_nop 0
	global_load_lds_dwordx4 v[216:217], off
	s_waitcnt vmcnt(8)
	s_waitcnt lgkmcnt(0)
	s_barrier
	s_setprio 1
	s_waitcnt lgkmcnt(0)
	v_mfma_f32_16x16x32_bf16 v[126:129], v[130:133], v[174:177], v[126:129]
	v_mfma_f32_16x16x32_bf16 v[122:125], v[138:141], v[174:177], v[122:125]
	v_mfma_f32_16x16x32_bf16 v[118:121], v[130:133], v[182:185], v[118:121]
	v_mfma_f32_16x16x32_bf16 v[114:117], v[138:141], v[182:185], v[114:117]
	v_mfma_f32_16x16x32_bf16 v[110:113], v[130:133], v[190:193], v[110:113]
	v_mfma_f32_16x16x32_bf16 v[106:109], v[138:141], v[190:193], v[106:109]
	v_mfma_f32_16x16x32_bf16 v[102:105], v[130:133], v[198:201], v[102:105]
	v_mfma_f32_16x16x32_bf16 v[98:101], v[138:141], v[198:201], v[98:101]
	v_mfma_f32_16x16x32_bf16 v[126:129], v[134:137], v[178:181], v[126:129]
	v_mfma_f32_16x16x32_bf16 v[122:125], v[142:145], v[178:181], v[122:125]
	v_mfma_f32_16x16x32_bf16 v[118:121], v[134:137], v[186:189], v[118:121]
	v_mfma_f32_16x16x32_bf16 v[114:117], v[142:145], v[186:189], v[114:117]
	v_mfma_f32_16x16x32_bf16 v[110:113], v[134:137], v[194:197], v[110:113]
	v_mfma_f32_16x16x32_bf16 v[106:109], v[142:145], v[194:197], v[106:109]
	v_mfma_f32_16x16x32_bf16 v[102:105], v[134:137], v[202:205], v[102:105]
	v_mfma_f32_16x16x32_bf16 v[98:101], v[142:145], v[202:205], v[98:101]
	v_mfma_f32_16x16x32_bf16 v[94:97], v[146:149], v[174:177], v[94:97]
	v_mfma_f32_16x16x32_bf16 v[90:93], v[154:157], v[174:177], v[90:93]
	v_mfma_f32_16x16x32_bf16 v[86:89], v[146:149], v[182:185], v[86:89]
	v_mfma_f32_16x16x32_bf16 v[82:85], v[154:157], v[182:185], v[82:85]
	v_mfma_f32_16x16x32_bf16 v[78:81], v[146:149], v[190:193], v[78:81]
	v_mfma_f32_16x16x32_bf16 v[74:77], v[154:157], v[190:193], v[74:77]
	v_mfma_f32_16x16x32_bf16 v[70:73], v[146:149], v[198:201], v[70:73]
	v_mfma_f32_16x16x32_bf16 v[66:69], v[154:157], v[198:201], v[66:69]
	v_mfma_f32_16x16x32_bf16 v[94:97], v[150:153], v[178:181], v[94:97]
	v_mfma_f32_16x16x32_bf16 v[90:93], v[158:161], v[178:181], v[90:93]
	v_mfma_f32_16x16x32_bf16 v[86:89], v[150:153], v[186:189], v[86:89]
	v_mfma_f32_16x16x32_bf16 v[82:85], v[158:161], v[186:189], v[82:85]
	v_mfma_f32_16x16x32_bf16 v[78:81], v[150:153], v[194:197], v[78:81]
	v_mfma_f32_16x16x32_bf16 v[74:77], v[158:161], v[194:197], v[74:77]
	v_mfma_f32_16x16x32_bf16 v[70:73], v[150:153], v[202:205], v[70:73]
	v_mfma_f32_16x16x32_bf16 v[66:69], v[158:161], v[202:205], v[66:69]
	s_setprio 0
	s_barrier
	s_mov_b32 m0, s66
	v_lshl_add_u64 v[170:171], v[170:171], 0, s[72:73]
	ds_read_b128 v[174:177], v173 offset:49152
	ds_read_b128 v[178:181], v173 offset:50176
	ds_read_b128 v[182:185], v173 offset:51200
	ds_read_b128 v[186:189], v173 offset:52224
	ds_read_b128 v[190:193], v173 offset:53248
	ds_read_b128 v[194:197], v173 offset:54272
	ds_read_b128 v[198:201], v173 offset:55296
	ds_read_b128 v[202:205], v173 offset:56320
	global_load_lds_dwordx4 v[170:171], off
	v_lshl_add_u64 v[170:171], v[206:207], 0, s[72:73]
	s_mov_b32 m0, s67
	s_nop 0
	global_load_lds_dwordx4 v[170:171], off
	v_lshl_add_u64 v[170:171], v[208:209], 0, s[72:73]
	s_mov_b32 m0, s81
	s_nop 0
	global_load_lds_dwordx4 v[170:171], off
	v_lshl_add_u64 v[170:171], v[210:211], 0, s[72:73]
	s_mov_b32 m0, s82
	s_nop 0
	global_load_lds_dwordx4 v[170:171], off
	v_lshl_add_u64 v[170:171], v[212:213], 0, s[72:73]
	s_mov_b32 m0, s70
	s_nop 0
	global_load_lds_dwordx4 v[170:171], off
	v_lshl_add_u64 v[170:171], v[214:215], 0, s[72:73]
	s_mov_b32 m0, s71
	s_nop 0
	global_load_lds_dwordx4 v[170:171], off
	s_waitcnt vmcnt(8)
	s_waitcnt lgkmcnt(0)
	s_barrier
	s_setprio 1
	s_waitcnt lgkmcnt(0)
	v_mfma_f32_16x16x32_bf16 v[62:65], v[130:133], v[174:177], v[62:65]
	v_mfma_f32_16x16x32_bf16 v[58:61], v[138:141], v[174:177], v[58:61]
	v_mfma_f32_16x16x32_bf16 v[54:57], v[130:133], v[182:185], v[54:57]
	v_mfma_f32_16x16x32_bf16 v[50:53], v[138:141], v[182:185], v[50:53]
	v_mfma_f32_16x16x32_bf16 v[46:49], v[130:133], v[190:193], v[46:49]
	v_mfma_f32_16x16x32_bf16 v[42:45], v[138:141], v[190:193], v[42:45]
	v_mfma_f32_16x16x32_bf16 v[38:41], v[130:133], v[198:201], v[38:41]
	v_mfma_f32_16x16x32_bf16 v[34:37], v[138:141], v[198:201], v[34:37]
	v_mfma_f32_16x16x32_bf16 v[62:65], v[134:137], v[178:181], v[62:65]
	v_mfma_f32_16x16x32_bf16 v[58:61], v[142:145], v[178:181], v[58:61]
	v_mfma_f32_16x16x32_bf16 v[54:57], v[134:137], v[186:189], v[54:57]
	v_mfma_f32_16x16x32_bf16 v[50:53], v[142:145], v[186:189], v[50:53]
	v_mfma_f32_16x16x32_bf16 v[46:49], v[134:137], v[194:197], v[46:49]
	v_mfma_f32_16x16x32_bf16 v[42:45], v[142:145], v[194:197], v[42:45]
	v_mfma_f32_16x16x32_bf16 v[38:41], v[134:137], v[202:205], v[38:41]
	v_mfma_f32_16x16x32_bf16 v[34:37], v[142:145], v[202:205], v[34:37]
	v_mfma_f32_16x16x32_bf16 v[30:33], v[146:149], v[174:177], v[30:33]
	v_mfma_f32_16x16x32_bf16 v[26:29], v[154:157], v[174:177], v[26:29]
	v_mfma_f32_16x16x32_bf16 v[22:25], v[146:149], v[182:185], v[22:25]
	v_mfma_f32_16x16x32_bf16 v[18:21], v[154:157], v[182:185], v[18:21]
	v_mfma_f32_16x16x32_bf16 v[14:17], v[146:149], v[190:193], v[14:17]
	v_mfma_f32_16x16x32_bf16 v[10:13], v[154:157], v[190:193], v[10:13]
	v_mfma_f32_16x16x32_bf16 v[6:9], v[146:149], v[198:201], v[6:9]
	v_mfma_f32_16x16x32_bf16 v[2:5], v[154:157], v[198:201], v[2:5]
	v_mfma_f32_16x16x32_bf16 v[30:33], v[150:153], v[178:181], v[30:33]
	v_mfma_f32_16x16x32_bf16 v[26:29], v[158:161], v[178:181], v[26:29]
	v_mfma_f32_16x16x32_bf16 v[22:25], v[150:153], v[186:189], v[22:25]
	v_mfma_f32_16x16x32_bf16 v[18:21], v[158:161], v[186:189], v[18:21]
	v_mfma_f32_16x16x32_bf16 v[14:17], v[150:153], v[194:197], v[14:17]
	v_mfma_f32_16x16x32_bf16 v[10:13], v[158:161], v[194:197], v[10:13]
	v_mfma_f32_16x16x32_bf16 v[6:9], v[150:153], v[202:205], v[6:9]
	v_mfma_f32_16x16x32_bf16 v[2:5], v[158:161], v[202:205], v[2:5]
	s_setprio 0
	s_barrier
	s_add_i32 s91, s91, 2
	s_add_u32 s30, s30, 0x100
	s_addc_u32 s31, s31, 0
	s_cmp_gt_u32 s91, 13
	s_cbranch_scc1 .LBB0_1016
.LBB0_1009:
	v_add_u32_e32 v130, s38, v172
	v_add_u32_e32 v142, s47, v172
	ds_read_b128 v[146:149], v130
	ds_read_b128 v[150:153], v130 offset:1024
	ds_read_b128 v[154:157], v130 offset:2048
	ds_read_b128 v[158:161], v130 offset:3072
	ds_read_b128 v[130:133], v142
	ds_read_b128 v[134:137], v142 offset:1024
	ds_read_b128 v[138:141], v142 offset:2048
	ds_read_b128 v[142:145], v142 offset:3072
	s_add_u32 s6, s18, s30
	s_addc_u32 s7, s19, s31
	v_lshl_add_u64 v[170:171], s[6:7], 0, v[218:219]
	v_lshl_add_u64 v[170:171], v[170:171], 0, s[64:65]
	s_add_i32 m0, s50, 0xc000
	v_mov_b32_e32 v167, v219
	ds_read_b128 v[174:177], v173
	ds_read_b128 v[178:181], v173 offset:1024
	ds_read_b128 v[182:185], v173 offset:2048
	ds_read_b128 v[186:189], v173 offset:3072
	ds_read_b128 v[190:193], v173 offset:4096
	ds_read_b128 v[194:197], v173 offset:5120
	ds_read_b128 v[198:201], v173 offset:6144
	ds_read_b128 v[202:205], v173 offset:7168
	global_load_lds_dwordx4 v[170:171], off
	v_lshl_add_u64 v[170:171], s[6:7], 0, v[166:167]
	v_lshl_add_u64 v[170:171], v[170:171], 0, s[64:65]
	s_add_i32 m0, s50, 0xe000
	s_nop 0
	global_load_lds_dwordx4 v[170:171], off
	s_waitcnt vmcnt(8)
	s_waitcnt lgkmcnt(0)
	s_barrier
	s_setprio 1
	s_waitcnt lgkmcnt(0)
	v_mfma_f32_16x16x32_bf16 v[126:129], v[146:149], v[174:177], v[126:129]
	v_mfma_f32_16x16x32_bf16 v[122:125], v[154:157], v[174:177], v[122:125]
	v_mfma_f32_16x16x32_bf16 v[118:121], v[146:149], v[182:185], v[118:121]
	v_mfma_f32_16x16x32_bf16 v[114:117], v[154:157], v[182:185], v[114:117]
	v_mfma_f32_16x16x32_bf16 v[110:113], v[146:149], v[190:193], v[110:113]
	v_mfma_f32_16x16x32_bf16 v[106:109], v[154:157], v[190:193], v[106:109]
	v_mfma_f32_16x16x32_bf16 v[102:105], v[146:149], v[198:201], v[102:105]
	v_mfma_f32_16x16x32_bf16 v[98:101], v[154:157], v[198:201], v[98:101]
	v_mfma_f32_16x16x32_bf16 v[126:129], v[150:153], v[178:181], v[126:129]
	v_mfma_f32_16x16x32_bf16 v[122:125], v[158:161], v[178:181], v[122:125]
	v_mfma_f32_16x16x32_bf16 v[118:121], v[150:153], v[186:189], v[118:121]
	v_mfma_f32_16x16x32_bf16 v[114:117], v[158:161], v[186:189], v[114:117]
	v_mfma_f32_16x16x32_bf16 v[110:113], v[150:153], v[194:197], v[110:113]
	v_mfma_f32_16x16x32_bf16 v[106:109], v[158:161], v[194:197], v[106:109]
	v_mfma_f32_16x16x32_bf16 v[102:105], v[150:153], v[202:205], v[102:105]
	v_mfma_f32_16x16x32_bf16 v[98:101], v[158:161], v[202:205], v[98:101]
	v_mfma_f32_16x16x32_bf16 v[94:97], v[130:133], v[174:177], v[94:97]
	s_cmpk_lg_i32 s30, 0x700
	v_mfma_f32_16x16x32_bf16 v[90:93], v[138:141], v[174:177], v[90:93]
	v_mfma_f32_16x16x32_bf16 v[86:89], v[130:133], v[182:185], v[86:89]
	v_mfma_f32_16x16x32_bf16 v[82:85], v[138:141], v[182:185], v[82:85]
	v_mfma_f32_16x16x32_bf16 v[78:81], v[130:133], v[190:193], v[78:81]
	v_mfma_f32_16x16x32_bf16 v[74:77], v[138:141], v[190:193], v[74:77]
	v_mfma_f32_16x16x32_bf16 v[70:73], v[130:133], v[198:201], v[70:73]
	v_mfma_f32_16x16x32_bf16 v[66:69], v[138:141], v[198:201], v[66:69]
	v_mfma_f32_16x16x32_bf16 v[94:97], v[134:137], v[178:181], v[94:97]
	v_mfma_f32_16x16x32_bf16 v[90:93], v[142:145], v[178:181], v[90:93]
	v_mfma_f32_16x16x32_bf16 v[86:89], v[134:137], v[186:189], v[86:89]
	v_mfma_f32_16x16x32_bf16 v[82:85], v[142:145], v[186:189], v[82:85]
	v_mfma_f32_16x16x32_bf16 v[78:81], v[134:137], v[194:197], v[78:81]
	v_mfma_f32_16x16x32_bf16 v[74:77], v[142:145], v[194:197], v[74:77]
	v_mfma_f32_16x16x32_bf16 v[70:73], v[134:137], v[202:205], v[70:73]
	v_mfma_f32_16x16x32_bf16 v[66:69], v[142:145], v[202:205], v[66:69]
	s_setprio 0
	s_barrier
	s_mov_b64 s[62:63], -1
	s_cbranch_scc0 .LBB0_1011
	s_add_u32 s6, s18, s30
	s_addc_u32 s7, s19, s31
	s_add_u32 s34, s6, 0x100
	s_addc_u32 s35, s7, 0
	s_add_u32 s56, s20, s30
	s_addc_u32 s57, s21, s31
	s_add_u32 s60, s56, 0x100
	s_addc_u32 s61, s57, 0
	s_add_u32 s6, s6, 0x40100
	s_addc_u32 s7, s7, 0
	s_add_u32 s56, s56, 0x40100
	s_addc_u32 s57, s57, 0
	s_mov_b64 s[62:63], 0

.LBB0_1262:
	v_add_u32_e32 v18, s27, v190
	v_add_u32_e32 v22, s43, v190
	ds_read_b128 v[10:13], v18
	ds_read_b128 v[14:17], v18 offset:1024
	ds_read_b128 v[24:27], v18 offset:2048
	ds_read_b128 v[28:31], v18 offset:3072
	ds_read_b128 v[182:185], v22
	ds_read_b128 v[186:189], v22 offset:1024
	ds_read_b128 v[192:195], v22 offset:2048
	ds_read_b128 v[196:199], v22 offset:3072
	s_add_i32 s94, s33, 1
	v_lshl_add_u64 v[178:179], s[6:7], 0, v[218:219]
	s_add_i32 s31, s46, 0xc000
	v_mov_b32_e32 v173, v219
	v_lshl_add_u64 v[20:21], v[178:179], 0, s[72:73]
	s_mov_b32 m0, s31
	v_lshl_add_u64 v[180:181], s[6:7], 0, v[172:173]
	s_add_i32 s30, s46, 0xe000
	ds_read_b128 v[2:5], v191
	ds_read_b128 v[6:9], v191 offset:1024
	ds_read_b128 v[38:41], v191 offset:2048
	ds_read_b128 v[42:45], v191 offset:3072
	ds_read_b128 v[46:49], v191 offset:4096
	ds_read_b128 v[50:53], v191 offset:5120
	ds_read_b128 v[54:57], v191 offset:6144
	ds_read_b128 v[58:61], v191 offset:7168
	global_load_lds_dwordx4 v[20:21], off
	v_lshl_add_u64 v[20:21], v[180:181], 0, s[72:73]
	s_mov_b32 m0, s30
	s_nop 0
	global_load_lds_dwordx4 v[20:21], off
	s_waitcnt vmcnt(8)
	s_waitcnt lgkmcnt(0)
	s_barrier
	s_setprio 1
	v_readlane_b32 s52, v255, 26
	v_readlane_b32 s53, v255, 27
	v_readlane_b32 s54, v255, 28
	v_readlane_b32 s55, v255, 29
	v_mov_b64_e32 v[34:35], s[52:53]
	s_nop 0
	v_mov_b64_e32 v[156:157], s[54:55]
	v_mov_b64_e32 v[148:149], s[54:55]
	v_mov_b64_e32 v[140:141], s[54:55]
	v_mov_b64_e32 v[132:133], s[54:55]
	v_mov_b64_e32 v[124:125], s[54:55]
	v_mov_b64_e32 v[116:117], s[54:55]
	v_mov_b64_e32 v[108:109], s[54:55]
	v_mov_b64_e32 v[100:101], s[54:55]
	v_mov_b64_e32 v[36:37], s[54:55]
	v_mov_b64_e32 v[154:155], s[52:53]
	v_mov_b64_e32 v[146:147], s[52:53]
	v_mov_b64_e32 v[138:139], s[52:53]
	v_mov_b64_e32 v[130:131], s[52:53]
	v_mov_b64_e32 v[122:123], s[52:53]
	v_mov_b64_e32 v[114:115], s[52:53]
	v_mov_b64_e32 v[106:107], s[52:53]
	v_mov_b64_e32 v[98:99], s[52:53]
	s_waitcnt lgkmcnt(0)
	v_mfma_scale_f32_16x16x128_f8f6f4 v[154:157], v[10:17], v[2:9], v[154:157], v232, v232 op_sel_hi:[0,0,0]
	v_mfma_scale_f32_16x16x128_f8f6f4 v[146:149], v[24:31], v[2:9], v[146:149], v232, v232 op_sel_hi:[0,0,0]
	v_mfma_scale_f32_16x16x128_f8f6f4 v[138:141], v[10:17], v[38:45], v[138:141], v232, v232 op_sel_hi:[0,0,0]
	v_mfma_scale_f32_16x16x128_f8f6f4 v[130:133], v[24:31], v[38:45], v[130:133], v232, v232 op_sel_hi:[0,0,0]
	v_mfma_scale_f32_16x16x128_f8f6f4 v[122:125], v[10:17], v[46:53], v[122:125], v232, v232 op_sel_hi:[0,0,0]
	v_mfma_scale_f32_16x16x128_f8f6f4 v[114:117], v[24:31], v[46:53], v[114:117], v232, v232 op_sel_hi:[0,0,0]
	v_mfma_scale_f32_16x16x128_f8f6f4 v[106:109], v[10:17], v[54:61], v[106:109], v232, v232 op_sel_hi:[0,0,0]
	v_mfma_scale_f32_16x16x128_f8f6f4 v[98:101], v[24:31], v[54:61], v[98:101], v232, v232 op_sel_hi:[0,0,0]
	v_mov_b64_e32 v[160:161], s[54:55]
	v_mov_b64_e32 v[152:153], s[54:55]
	v_mov_b64_e32 v[144:145], s[54:55]
	v_mov_b64_e32 v[136:137], s[54:55]
	v_mov_b64_e32 v[128:129], s[54:55]
	v_mov_b64_e32 v[120:121], s[54:55]
	v_mov_b64_e32 v[112:113], s[54:55]
	v_mov_b64_e32 v[104:105], s[54:55]
	v_mov_b64_e32 v[158:159], s[52:53]
	v_mov_b64_e32 v[150:151], s[52:53]
	v_mov_b64_e32 v[142:143], s[52:53]
	v_mov_b64_e32 v[134:135], s[52:53]
	v_mov_b64_e32 v[126:127], s[52:53]
	v_mov_b64_e32 v[118:119], s[52:53]
	v_mov_b64_e32 v[110:111], s[52:53]
	v_mov_b64_e32 v[102:103], s[52:53]
	v_mfma_scale_f32_16x16x128_f8f6f4 v[158:161], v[182:189], v[2:9], v[158:161], v232, v232 op_sel_hi:[0,0,0]
	v_mfma_scale_f32_16x16x128_f8f6f4 v[150:153], v[192:199], v[2:9], v[150:153], v232, v232 op_sel_hi:[0,0,0]
	v_mfma_scale_f32_16x16x128_f8f6f4 v[142:145], v[182:189], v[38:45], v[142:145], v232, v232 op_sel_hi:[0,0,0]
	v_mfma_scale_f32_16x16x128_f8f6f4 v[134:137], v[192:199], v[38:45], v[134:137], v232, v232 op_sel_hi:[0,0,0]
	v_mfma_scale_f32_16x16x128_f8f6f4 v[126:129], v[182:189], v[46:53], v[126:129], v232, v232 op_sel_hi:[0,0,0]
	v_mfma_scale_f32_16x16x128_f8f6f4 v[118:121], v[192:199], v[46:53], v[118:121], v232, v232 op_sel_hi:[0,0,0]
	v_mfma_scale_f32_16x16x128_f8f6f4 v[110:113], v[182:189], v[54:61], v[110:113], v232, v232 op_sel_hi:[0,0,0]
	v_mfma_scale_f32_16x16x128_f8f6f4 v[102:105], v[192:199], v[54:61], v[102:105], v232, v232 op_sel_hi:[0,0,0]
	s_setprio 0
	s_barrier
	v_mov_b32_e32 v165, v219
	v_lshl_add_u64 v[2:3], s[28:29], 0, v[164:165]
	s_mov_b32 m0, s41
	v_lshl_add_u64 v[4:5], v[2:3], 0, s[76:77]
	v_mov_b32_e32 v175, v219
	ds_read_b128 v[200:203], v191 offset:16384
	ds_read_b128 v[204:207], v191 offset:17408
	ds_read_b128 v[208:211], v191 offset:18432
	ds_read_b128 v[212:215], v191 offset:19456
	ds_read_b128 v[222:225], v191 offset:20480
	ds_read_b128 v[226:229], v191 offset:21504
	ds_read_b128 v[244:247], v191 offset:22528
	ds_read_b128 v[248:251], v191 offset:23552
	global_load_lds_dwordx4 v[4:5], off
	v_lshl_add_u64 v[4:5], s[28:29], 0, v[174:175]
	s_add_u32 s2, s28, 0x20100
	v_lshl_add_u64 v[6:7], v[4:5], 0, s[76:77]
	s_mov_b32 m0, s42
	s_addc_u32 s3, s29, 0
	global_load_lds_dwordx4 v[6:7], off
	s_mov_b32 m0, s44
	v_mov_b32_e32 v169, v219
	global_load_lds_dwordx4 v164, s[2:3]
	s_mov_b32 m0, s45
	v_lshl_add_u64 v[6:7], s[6:7], 0, v[168:169]
	global_load_lds_dwordx4 v174, s[2:3]
	v_lshl_add_u64 v[8:9], v[6:7], 0, s[76:77]
	s_mov_b32 m0, s46
	v_mov_b32_e32 v167, v219
	global_load_lds_dwordx4 v[8:9], off
	v_lshl_add_u64 v[8:9], s[6:7], 0, v[166:167]
	v_lshl_add_u64 v[20:21], v[8:9], 0, s[76:77]
	s_mov_b32 m0, s47
	s_nop 0
	global_load_lds_dwordx4 v[20:21], off
	s_waitcnt vmcnt(8)
	s_waitcnt lgkmcnt(0)
	s_barrier
	s_setprio 1
	v_mov_b64_e32 v[92:93], s[54:55]
	v_mov_b64_e32 v[84:85], s[54:55]
	v_mov_b64_e32 v[76:77], s[54:55]
	v_mov_b64_e32 v[68:69], s[54:55]
	v_mov_b64_e32 v[60:61], s[54:55]
	v_mov_b64_e32 v[50:51], s[52:53]
	v_mov_b64_e32 v[42:43], s[52:53]
	v_mov_b64_e32 v[38:39], s[52:53]
	v_mov_b64_e32 v[90:91], s[52:53]
	v_mov_b64_e32 v[82:83], s[52:53]
	v_mov_b64_e32 v[74:75], s[52:53]
	v_mov_b64_e32 v[66:67], s[52:53]
	v_mov_b64_e32 v[58:59], s[52:53]
	v_mov_b64_e32 v[52:53], s[54:55]
	v_mov_b64_e32 v[44:45], s[54:55]
	v_mov_b64_e32 v[40:41], s[54:55]
	s_waitcnt lgkmcnt(0)
	v_mfma_scale_f32_16x16x128_f8f6f4 v[90:93], v[10:17], v[200:207], v[90:93], v232, v232 op_sel_hi:[0,0,0]
	v_mfma_scale_f32_16x16x128_f8f6f4 v[82:85], v[24:31], v[200:207], v[82:85], v232, v232 op_sel_hi:[0,0,0]
	v_mfma_scale_f32_16x16x128_f8f6f4 v[74:77], v[10:17], v[208:215], v[74:77], v232, v232 op_sel_hi:[0,0,0]
	v_mfma_scale_f32_16x16x128_f8f6f4 v[66:69], v[24:31], v[208:215], v[66:69], v232, v232 op_sel_hi:[0,0,0]
	v_mfma_scale_f32_16x16x128_f8f6f4 v[58:61], v[10:17], v[222:229], v[58:61], v232, v232 op_sel_hi:[0,0,0]
	v_mfma_scale_f32_16x16x128_f8f6f4 v[50:53], v[24:31], v[222:229], v[50:53], v232, v232 op_sel_hi:[0,0,0]
	v_mfma_scale_f32_16x16x128_f8f6f4 v[42:45], v[10:17], v[244:251], v[42:45], v232, v232 op_sel_hi:[0,0,0]
	v_mfma_scale_f32_16x16x128_f8f6f4 v[38:41], v[24:31], v[244:251], v[38:41], v232, v232 op_sel_hi:[0,0,0]
	v_mov_b64_e32 v[96:97], s[54:55]
	v_mov_b64_e32 v[88:89], s[54:55]
	v_mov_b64_e32 v[80:81], s[54:55]
	v_mov_b64_e32 v[72:73], s[54:55]
	v_mov_b64_e32 v[64:65], s[54:55]
	v_mov_b64_e32 v[56:57], s[54:55]
	v_mov_b64_e32 v[46:47], s[52:53]
	v_mov_b64_e32 v[94:95], s[52:53]
	v_mov_b64_e32 v[86:87], s[52:53]
	v_mov_b64_e32 v[78:79], s[52:53]
	v_mov_b64_e32 v[70:71], s[52:53]
	v_mov_b64_e32 v[62:63], s[52:53]
	v_mov_b64_e32 v[54:55], s[52:53]
	v_mov_b64_e32 v[48:49], s[54:55]
	v_mfma_scale_f32_16x16x128_f8f6f4 v[94:97], v[182:189], v[200:207], v[94:97], v232, v232 op_sel_hi:[0,0,0]
	v_mfma_scale_f32_16x16x128_f8f6f4 v[86:89], v[192:199], v[200:207], v[86:89], v232, v232 op_sel_hi:[0,0,0]
	v_mfma_scale_f32_16x16x128_f8f6f4 v[78:81], v[182:189], v[208:215], v[78:81], v232, v232 op_sel_hi:[0,0,0]
	v_mfma_scale_f32_16x16x128_f8f6f4 v[70:73], v[192:199], v[208:215], v[70:73], v232, v232 op_sel_hi:[0,0,0]
	v_mfma_scale_f32_16x16x128_f8f6f4 v[62:65], v[182:189], v[222:229], v[62:65], v232, v232 op_sel_hi:[0,0,0]
	v_mfma_scale_f32_16x16x128_f8f6f4 v[54:57], v[192:199], v[222:229], v[54:57], v232, v232 op_sel_hi:[0,0,0]
	v_mfma_scale_f32_16x16x128_f8f6f4 v[46:49], v[182:189], v[244:251], v[46:49], v232, v232 op_sel_hi:[0,0,0]
	v_mfma_scale_f32_16x16x128_f8f6f4 v[34:37], v[192:199], v[244:251], v[34:37], v232, v232 op_sel_hi:[0,0,0]
	s_setprio 0
	s_barrier
	v_add_u32_e32 v192, s50, v190
	v_add_u32_e32 v193, s61, v190
	ds_read_b128 v[10:13], v192
	ds_read_b128 v[14:17], v192 offset:1024
	ds_read_b128 v[24:27], v192 offset:2048
	ds_read_b128 v[28:31], v192 offset:3072
	ds_read_b128 v[182:185], v193
	ds_read_b128 v[186:189], v193 offset:1024
	ds_read_b128 v[194:197], v193 offset:2048
	ds_read_b128 v[198:201], v193 offset:3072
	s_mov_b32 m0, s48
	v_lshl_add_u64 v[20:21], v[178:179], 0, s[76:77]
	ds_read_b128 v[202:205], v191 offset:32768
	ds_read_b128 v[206:209], v191 offset:33792
	ds_read_b128 v[210:213], v191 offset:34816
	ds_read_b128 v[214:217], v191 offset:35840
	ds_read_b128 v[222:225], v191 offset:36864
	ds_read_b128 v[226:229], v191 offset:37888
	ds_read_b128 v[244:247], v191 offset:38912
	ds_read_b128 v[248:251], v191 offset:39936
	global_load_lds_dwordx4 v[20:21], off
	v_lshl_add_u64 v[20:21], v[180:181], 0, s[76:77]
	s_mov_b32 m0, s49
	s_nop 0
	global_load_lds_dwordx4 v[20:21], off
	s_waitcnt vmcnt(8)
	s_waitcnt lgkmcnt(0)
	s_barrier
	s_setprio 1
	s_waitcnt lgkmcnt(0)
	v_mfma_scale_f32_16x16x128_f8f6f4 v[154:157], v[10:17], v[202:209], v[154:157], v232, v232 op_sel_hi:[0,0,0]
	v_mfma_scale_f32_16x16x128_f8f6f4 v[146:149], v[24:31], v[202:209], v[146:149], v232, v232 op_sel_hi:[0,0,0]
	v_mfma_scale_f32_16x16x128_f8f6f4 v[138:141], v[10:17], v[210:217], v[138:141], v232, v232 op_sel_hi:[0,0,0]
	v_mfma_scale_f32_16x16x128_f8f6f4 v[130:133], v[24:31], v[210:217], v[130:133], v232, v232 op_sel_hi:[0,0,0]
	v_mfma_scale_f32_16x16x128_f8f6f4 v[122:125], v[10:17], v[222:229], v[122:125], v232, v232 op_sel_hi:[0,0,0]
	v_mfma_scale_f32_16x16x128_f8f6f4 v[114:117], v[24:31], v[222:229], v[114:117], v232, v232 op_sel_hi:[0,0,0]
	v_mfma_scale_f32_16x16x128_f8f6f4 v[106:109], v[10:17], v[244:251], v[106:109], v232, v232 op_sel_hi:[0,0,0]
	v_mfma_scale_f32_16x16x128_f8f6f4 v[98:101], v[24:31], v[244:251], v[98:101], v232, v232 op_sel_hi:[0,0,0]
	v_mfma_scale_f32_16x16x128_f8f6f4 v[158:161], v[182:189], v[202:209], v[158:161], v232, v232 op_sel_hi:[0,0,0]
	v_mfma_scale_f32_16x16x128_f8f6f4 v[150:153], v[194:201], v[202:209], v[150:153], v232, v232 op_sel_hi:[0,0,0]
	v_mfma_scale_f32_16x16x128_f8f6f4 v[142:145], v[182:189], v[210:217], v[142:145], v232, v232 op_sel_hi:[0,0,0]
	v_mfma_scale_f32_16x16x128_f8f6f4 v[134:137], v[194:201], v[210:217], v[134:137], v232, v232 op_sel_hi:[0,0,0]
	v_mfma_scale_f32_16x16x128_f8f6f4 v[126:129], v[182:189], v[222:229], v[126:129], v232, v232 op_sel_hi:[0,0,0]
	v_mfma_scale_f32_16x16x128_f8f6f4 v[118:121], v[194:201], v[222:229], v[118:121], v232, v232 op_sel_hi:[0,0,0]
	v_mfma_scale_f32_16x16x128_f8f6f4 v[110:113], v[182:189], v[244:251], v[110:113], v232, v232 op_sel_hi:[0,0,0]
	v_mfma_scale_f32_16x16x128_f8f6f4 v[102:105], v[194:201], v[244:251], v[102:105], v232, v232 op_sel_hi:[0,0,0]
	s_setprio 0
	s_barrier
	s_mov_b64 s[52:53], 0x180
	s_mov_b32 m0, s51
	v_lshl_add_u64 v[20:21], v[2:3], 0, s[52:53]
	ds_read_b128 v[202:205], v191 offset:49152
	ds_read_b128 v[206:209], v191 offset:50176
	ds_read_b128 v[210:213], v191 offset:51200
	ds_read_b128 v[214:217], v191 offset:52224
	ds_read_b128 v[222:225], v191 offset:53248
	ds_read_b128 v[226:229], v191 offset:54272
	ds_read_b128 v[244:247], v191 offset:55296
	ds_read_b128 v[248:251], v191 offset:56320
	global_load_lds_dwordx4 v[20:21], off
	v_lshl_add_u64 v[20:21], v[4:5], 0, s[52:53]
	s_mov_b32 m0, s56
	s_add_u32 s2, s28, 0x20180
	global_load_lds_dwordx4 v[20:21], off
	s_addc_u32 s3, s29, 0
	s_mov_b32 m0, s62
	v_lshl_add_u64 v[20:21], v[6:7], 0, s[52:53]
	global_load_lds_dwordx4 v164, s[2:3]
	s_mov_b32 m0, s63
	s_nop 0
	global_load_lds_dwordx4 v174, s[2:3]
	s_mov_b32 m0, s57
	s_nop 0
	global_load_lds_dwordx4 v[20:21], off
	v_lshl_add_u64 v[20:21], v[8:9], 0, s[52:53]
	s_mov_b32 m0, s60
	s_nop 0
	global_load_lds_dwordx4 v[20:21], off
	s_waitcnt vmcnt(8)
	s_waitcnt lgkmcnt(0)
	s_barrier
	s_setprio 1
	s_waitcnt lgkmcnt(0)
	v_mfma_scale_f32_16x16x128_f8f6f4 v[90:93], v[10:17], v[202:209], v[90:93], v232, v232 op_sel_hi:[0,0,0]
	v_mfma_scale_f32_16x16x128_f8f6f4 v[82:85], v[24:31], v[202:209], v[82:85], v232, v232 op_sel_hi:[0,0,0]
	v_mfma_scale_f32_16x16x128_f8f6f4 v[74:77], v[10:17], v[210:217], v[74:77], v232, v232 op_sel_hi:[0,0,0]
	v_mfma_scale_f32_16x16x128_f8f6f4 v[66:69], v[24:31], v[210:217], v[66:69], v232, v232 op_sel_hi:[0,0,0]
	v_mfma_scale_f32_16x16x128_f8f6f4 v[58:61], v[10:17], v[222:229], v[58:61], v232, v232 op_sel_hi:[0,0,0]
	v_mfma_scale_f32_16x16x128_f8f6f4 v[50:53], v[24:31], v[222:229], v[50:53], v232, v232 op_sel_hi:[0,0,0]
	v_mfma_scale_f32_16x16x128_f8f6f4 v[42:45], v[10:17], v[244:251], v[42:45], v232, v232 op_sel_hi:[0,0,0]
	v_mfma_scale_f32_16x16x128_f8f6f4 v[38:41], v[24:31], v[244:251], v[38:41], v232, v232 op_sel_hi:[0,0,0]
	v_mfma_scale_f32_16x16x128_f8f6f4 v[94:97], v[182:189], v[202:209], v[94:97], v232, v232 op_sel_hi:[0,0,0]
	v_mfma_scale_f32_16x16x128_f8f6f4 v[86:89], v[194:201], v[202:209], v[86:89], v232, v232 op_sel_hi:[0,0,0]
	v_mfma_scale_f32_16x16x128_f8f6f4 v[78:81], v[182:189], v[210:217], v[78:81], v232, v232 op_sel_hi:[0,0,0]
	v_mfma_scale_f32_16x16x128_f8f6f4 v[70:73], v[194:201], v[210:217], v[70:73], v232, v232 op_sel_hi:[0,0,0]
	v_mfma_scale_f32_16x16x128_f8f6f4 v[62:65], v[182:189], v[222:229], v[62:65], v232, v232 op_sel_hi:[0,0,0]
	v_mfma_scale_f32_16x16x128_f8f6f4 v[54:57], v[194:201], v[222:229], v[54:57], v232, v232 op_sel_hi:[0,0,0]
	v_mfma_scale_f32_16x16x128_f8f6f4 v[46:49], v[182:189], v[244:251], v[46:49], v232, v232 op_sel_hi:[0,0,0]
	v_mfma_scale_f32_16x16x128_f8f6f4 v[34:37], v[194:201], v[244:251], v[34:37], v232, v232 op_sel_hi:[0,0,0]
	s_setprio 0
	s_barrier
	s_andn2_b64 vcc, exec, s[8:9]
	s_cbranch_vccnz .LBB0_1266
	s_and_b64 vcc, exec, s[4:5]
	s_mov_b64 s[2:3], 0
	s_cbranch_vccnz .LBB0_1267
	v_mov_b32_e32 v10, s88
	ds_read_b128 v[10:13], v10
	s_movk_i32 s70, 0xe00
	s_waitcnt lgkmcnt(0)
	v_readfirstlane_b32 s23, v10
	s_cmp_lt_i32 s23, 0
	v_readfirstlane_b32 s2, v12
	s_cbranch_scc1 .LBB0_1287
	s_ashr_i32 s90, s2, 16
	s_mov_b32 s22, s23
	s_branch .LBB0_1268

.LBB0_1269:
	ds_read_b128 v[10:13], v18
	ds_read_b128 v[14:17], v18 offset:1024
	ds_read_b128 v[24:27], v18 offset:2048
	ds_read_b128 v[28:31], v18 offset:3072
	ds_read_b128 v[182:185], v22
	ds_read_b128 v[186:189], v22 offset:1024
	ds_read_b128 v[194:197], v22 offset:2048
	ds_read_b128 v[198:201], v22 offset:3072
	s_mov_b64 s[2:3], 0x180
	s_mov_b32 m0, s31
	v_lshl_add_u64 v[20:21], v[178:179], 0, s[2:3]
	ds_read_b128 v[202:205], v191
	ds_read_b128 v[206:209], v191 offset:1024
	ds_read_b128 v[210:213], v191 offset:2048
	ds_read_b128 v[214:217], v191 offset:3072
	ds_read_b128 v[222:225], v191 offset:4096
	ds_read_b128 v[226:229], v191 offset:5120
	ds_read_b128 v[244:247], v191 offset:6144
	ds_read_b128 v[248:251], v191 offset:7168
	global_load_lds_dwordx4 v[20:21], off
	v_lshl_add_u64 v[20:21], v[180:181], 0, s[2:3]
	s_mov_b32 m0, s30
	s_nop 0
	global_load_lds_dwordx4 v[20:21], off
	s_waitcnt vmcnt(8)
	s_waitcnt lgkmcnt(0)
	s_barrier
	s_setprio 1
	s_waitcnt lgkmcnt(0)
	v_mfma_scale_f32_16x16x128_f8f6f4 v[154:157], v[10:17], v[202:209], v[154:157], v232, v232 op_sel_hi:[0,0,0]
	v_mfma_scale_f32_16x16x128_f8f6f4 v[146:149], v[24:31], v[202:209], v[146:149], v232, v232 op_sel_hi:[0,0,0]
	v_mfma_scale_f32_16x16x128_f8f6f4 v[138:141], v[10:17], v[210:217], v[138:141], v232, v232 op_sel_hi:[0,0,0]
	v_mfma_scale_f32_16x16x128_f8f6f4 v[130:133], v[24:31], v[210:217], v[130:133], v232, v232 op_sel_hi:[0,0,0]
	v_mfma_scale_f32_16x16x128_f8f6f4 v[122:125], v[10:17], v[222:229], v[122:125], v232, v232 op_sel_hi:[0,0,0]
	v_mfma_scale_f32_16x16x128_f8f6f4 v[114:117], v[24:31], v[222:229], v[114:117], v232, v232 op_sel_hi:[0,0,0]
	v_mfma_scale_f32_16x16x128_f8f6f4 v[106:109], v[10:17], v[244:251], v[106:109], v232, v232 op_sel_hi:[0,0,0]
	v_mfma_scale_f32_16x16x128_f8f6f4 v[98:101], v[24:31], v[244:251], v[98:101], v232, v232 op_sel_hi:[0,0,0]
	v_mfma_scale_f32_16x16x128_f8f6f4 v[158:161], v[182:189], v[202:209], v[158:161], v232, v232 op_sel_hi:[0,0,0]
	v_mfma_scale_f32_16x16x128_f8f6f4 v[150:153], v[194:201], v[202:209], v[150:153], v232, v232 op_sel_hi:[0,0,0]
	v_mfma_scale_f32_16x16x128_f8f6f4 v[142:145], v[182:189], v[210:217], v[142:145], v232, v232 op_sel_hi:[0,0,0]
	v_mfma_scale_f32_16x16x128_f8f6f4 v[134:137], v[194:201], v[210:217], v[134:137], v232, v232 op_sel_hi:[0,0,0]
	v_mfma_scale_f32_16x16x128_f8f6f4 v[126:129], v[182:189], v[222:229], v[126:129], v232, v232 op_sel_hi:[0,0,0]
	v_mfma_scale_f32_16x16x128_f8f6f4 v[118:121], v[194:201], v[222:229], v[118:121], v232, v232 op_sel_hi:[0,0,0]
	v_mfma_scale_f32_16x16x128_f8f6f4 v[110:113], v[182:189], v[244:251], v[110:113], v232, v232 op_sel_hi:[0,0,0]
	v_mfma_scale_f32_16x16x128_f8f6f4 v[102:105], v[194:201], v[244:251], v[102:105], v232, v232 op_sel_hi:[0,0,0]
	s_setprio 0
	s_barrier
	s_mov_b32 m0, s41
	s_add_u32 s2, s28, 0x20200
	v_lshl_add_u64 v[20:21], v[2:3], 0, s[66:67]
	s_addc_u32 s3, s29, 0
	ds_read_b128 v[202:205], v191 offset:16384
	ds_read_b128 v[206:209], v191 offset:17408
	ds_read_b128 v[210:213], v191 offset:18432
	ds_read_b128 v[214:217], v191 offset:19456
	ds_read_b128 v[222:225], v191 offset:20480
	ds_read_b128 v[226:229], v191 offset:21504
	ds_read_b128 v[244:247], v191 offset:22528
	ds_read_b128 v[248:251], v191 offset:23552
	global_load_lds_dwordx4 v[20:21], off
	v_lshl_add_u64 v[20:21], v[4:5], 0, s[66:67]
	s_mov_b32 m0, s42
	s_nop 0
	global_load_lds_dwordx4 v[20:21], off
	v_lshl_add_u64 v[20:21], s[2:3], 0, v[164:165]
	s_mov_b32 m0, s44
	s_nop 0
	global_load_lds_dwordx4 v[20:21], off
	v_lshl_add_u64 v[20:21], s[2:3], 0, v[174:175]
	s_mov_b32 m0, s45
	s_nop 0
	global_load_lds_dwordx4 v[20:21], off
	v_lshl_add_u64 v[20:21], v[6:7], 0, s[66:67]
	s_mov_b32 m0, s46
	s_nop 0
	global_load_lds_dwordx4 v[20:21], off
	v_lshl_add_u64 v[20:21], v[8:9], 0, s[66:67]
	s_mov_b32 m0, s47
	s_nop 0
	global_load_lds_dwordx4 v[20:21], off
	s_waitcnt vmcnt(8)
	s_waitcnt lgkmcnt(0)
	s_barrier
	s_setprio 1
	s_waitcnt lgkmcnt(0)
	v_mfma_scale_f32_16x16x128_f8f6f4 v[90:93], v[10:17], v[202:209], v[90:93], v232, v232 op_sel_hi:[0,0,0]
	v_mfma_scale_f32_16x16x128_f8f6f4 v[82:85], v[24:31], v[202:209], v[82:85], v232, v232 op_sel_hi:[0,0,0]
	v_mfma_scale_f32_16x16x128_f8f6f4 v[74:77], v[10:17], v[210:217], v[74:77], v232, v232 op_sel_hi:[0,0,0]
	v_mfma_scale_f32_16x16x128_f8f6f4 v[66:69], v[24:31], v[210:217], v[66:69], v232, v232 op_sel_hi:[0,0,0]
	v_mfma_scale_f32_16x16x128_f8f6f4 v[58:61], v[10:17], v[222:229], v[58:61], v232, v232 op_sel_hi:[0,0,0]
	v_mfma_scale_f32_16x16x128_f8f6f4 v[50:53], v[24:31], v[222:229], v[50:53], v232, v232 op_sel_hi:[0,0,0]
	v_mfma_scale_f32_16x16x128_f8f6f4 v[42:45], v[10:17], v[244:251], v[42:45], v232, v232 op_sel_hi:[0,0,0]
	v_mfma_scale_f32_16x16x128_f8f6f4 v[38:41], v[24:31], v[244:251], v[38:41], v232, v232 op_sel_hi:[0,0,0]
	v_mfma_scale_f32_16x16x128_f8f6f4 v[94:97], v[182:189], v[202:209], v[94:97], v232, v232 op_sel_hi:[0,0,0]
	v_mfma_scale_f32_16x16x128_f8f6f4 v[86:89], v[194:201], v[202:209], v[86:89], v232, v232 op_sel_hi:[0,0,0]
	v_mfma_scale_f32_16x16x128_f8f6f4 v[78:81], v[182:189], v[210:217], v[78:81], v232, v232 op_sel_hi:[0,0,0]
	v_mfma_scale_f32_16x16x128_f8f6f4 v[70:73], v[194:201], v[210:217], v[70:73], v232, v232 op_sel_hi:[0,0,0]
	v_mfma_scale_f32_16x16x128_f8f6f4 v[62:65], v[182:189], v[222:229], v[62:65], v232, v232 op_sel_hi:[0,0,0]
	v_mfma_scale_f32_16x16x128_f8f6f4 v[54:57], v[194:201], v[222:229], v[54:57], v232, v232 op_sel_hi:[0,0,0]
	v_mfma_scale_f32_16x16x128_f8f6f4 v[46:49], v[182:189], v[244:251], v[46:49], v232, v232 op_sel_hi:[0,0,0]
	v_mfma_scale_f32_16x16x128_f8f6f4 v[34:37], v[194:201], v[244:251], v[34:37], v232, v232 op_sel_hi:[0,0,0]
	s_setprio 0
	s_barrier
	ds_read_b128 v[10:13], v192
	ds_read_b128 v[14:17], v192 offset:1024
	ds_read_b128 v[24:27], v192 offset:2048
	ds_read_b128 v[28:31], v192 offset:3072
	ds_read_b128 v[182:185], v193
	ds_read_b128 v[186:189], v193 offset:1024
	ds_read_b128 v[194:197], v193 offset:2048
	ds_read_b128 v[198:201], v193 offset:3072
	s_mov_b32 m0, s48
	v_lshl_add_u64 v[20:21], v[178:179], 0, s[66:67]
	ds_read_b128 v[202:205], v191 offset:32768
	ds_read_b128 v[206:209], v191 offset:33792
	ds_read_b128 v[210:213], v191 offset:34816
	ds_read_b128 v[214:217], v191 offset:35840
	ds_read_b128 v[222:225], v191 offset:36864
	ds_read_b128 v[226:229], v191 offset:37888
	ds_read_b128 v[244:247], v191 offset:38912
	ds_read_b128 v[248:251], v191 offset:39936
	global_load_lds_dwordx4 v[20:21], off
	v_lshl_add_u64 v[20:21], v[180:181], 0, s[66:67]
	s_mov_b32 m0, s49
	s_nop 0
	global_load_lds_dwordx4 v[20:21], off
	s_waitcnt vmcnt(8)
	s_waitcnt lgkmcnt(0)
	s_barrier
	s_setprio 1
	s_waitcnt lgkmcnt(0)
	v_mfma_scale_f32_16x16x128_f8f6f4 v[154:157], v[10:17], v[202:209], v[154:157], v232, v232 op_sel_hi:[0,0,0]
	v_mfma_scale_f32_16x16x128_f8f6f4 v[146:149], v[24:31], v[202:209], v[146:149], v232, v232 op_sel_hi:[0,0,0]
	v_mfma_scale_f32_16x16x128_f8f6f4 v[138:141], v[10:17], v[210:217], v[138:141], v232, v232 op_sel_hi:[0,0,0]
	v_mfma_scale_f32_16x16x128_f8f6f4 v[130:133], v[24:31], v[210:217], v[130:133], v232, v232 op_sel_hi:[0,0,0]
	v_mfma_scale_f32_16x16x128_f8f6f4 v[122:125], v[10:17], v[222:229], v[122:125], v232, v232 op_sel_hi:[0,0,0]
	v_mfma_scale_f32_16x16x128_f8f6f4 v[114:117], v[24:31], v[222:229], v[114:117], v232, v232 op_sel_hi:[0,0,0]
	v_mfma_scale_f32_16x16x128_f8f6f4 v[106:109], v[10:17], v[244:251], v[106:109], v232, v232 op_sel_hi:[0,0,0]
	v_mfma_scale_f32_16x16x128_f8f6f4 v[98:101], v[24:31], v[244:251], v[98:101], v232, v232 op_sel_hi:[0,0,0]
	v_mfma_scale_f32_16x16x128_f8f6f4 v[158:161], v[182:189], v[202:209], v[158:161], v232, v232 op_sel_hi:[0,0,0]
	v_mfma_scale_f32_16x16x128_f8f6f4 v[150:153], v[194:201], v[202:209], v[150:153], v232, v232 op_sel_hi:[0,0,0]
	v_mfma_scale_f32_16x16x128_f8f6f4 v[142:145], v[182:189], v[210:217], v[142:145], v232, v232 op_sel_hi:[0,0,0]
	v_mfma_scale_f32_16x16x128_f8f6f4 v[134:137], v[194:201], v[210:217], v[134:137], v232, v232 op_sel_hi:[0,0,0]
	v_mfma_scale_f32_16x16x128_f8f6f4 v[126:129], v[182:189], v[222:229], v[126:129], v232, v232 op_sel_hi:[0,0,0]
	v_mfma_scale_f32_16x16x128_f8f6f4 v[118:121], v[194:201], v[222:229], v[118:121], v232, v232 op_sel_hi:[0,0,0]
	v_mfma_scale_f32_16x16x128_f8f6f4 v[110:113], v[182:189], v[244:251], v[110:113], v232, v232 op_sel_hi:[0,0,0]
	v_mfma_scale_f32_16x16x128_f8f6f4 v[102:105], v[194:201], v[244:251], v[102:105], v232, v232 op_sel_hi:[0,0,0]
	s_setprio 0
	s_barrier
	s_mov_b64 s[52:53], 0x280
	s_mov_b32 m0, s51
	v_lshl_add_u64 v[20:21], v[2:3], 0, s[52:53]
	s_add_u32 s2, s28, 0x20280
	ds_read_b128 v[202:205], v191 offset:49152
	ds_read_b128 v[206:209], v191 offset:50176
	ds_read_b128 v[210:213], v191 offset:51200
	ds_read_b128 v[214:217], v191 offset:52224
	ds_read_b128 v[222:225], v191 offset:53248
	ds_read_b128 v[226:229], v191 offset:54272
	ds_read_b128 v[244:247], v191 offset:55296
	ds_read_b128 v[248:251], v191 offset:56320
	global_load_lds_dwordx4 v[20:21], off
	v_lshl_add_u64 v[20:21], v[4:5], 0, s[52:53]
	s_mov_b32 m0, s56
	s_addc_u32 s3, s29, 0
	global_load_lds_dwordx4 v[20:21], off
	v_lshl_add_u64 v[20:21], s[2:3], 0, v[164:165]
	s_mov_b32 m0, s62
	s_nop 0
	global_load_lds_dwordx4 v[20:21], off
	v_lshl_add_u64 v[20:21], s[2:3], 0, v[174:175]
	s_mov_b32 m0, s63
	s_nop 0
	global_load_lds_dwordx4 v[20:21], off
	v_lshl_add_u64 v[20:21], v[6:7], 0, s[52:53]
	s_mov_b32 m0, s57
	s_nop 0
	global_load_lds_dwordx4 v[20:21], off
	v_lshl_add_u64 v[20:21], v[8:9], 0, s[52:53]
	s_mov_b32 m0, s60
	s_nop 0
	global_load_lds_dwordx4 v[20:21], off
	s_waitcnt vmcnt(8)
	s_waitcnt lgkmcnt(0)
	s_barrier
	s_setprio 1
	s_waitcnt lgkmcnt(0)
	v_mfma_scale_f32_16x16x128_f8f6f4 v[90:93], v[10:17], v[202:209], v[90:93], v232, v232 op_sel_hi:[0,0,0]
	v_mfma_scale_f32_16x16x128_f8f6f4 v[82:85], v[24:31], v[202:209], v[82:85], v232, v232 op_sel_hi:[0,0,0]
	v_mfma_scale_f32_16x16x128_f8f6f4 v[74:77], v[10:17], v[210:217], v[74:77], v232, v232 op_sel_hi:[0,0,0]
	v_mfma_scale_f32_16x16x128_f8f6f4 v[66:69], v[24:31], v[210:217], v[66:69], v232, v232 op_sel_hi:[0,0,0]
	v_mfma_scale_f32_16x16x128_f8f6f4 v[58:61], v[10:17], v[222:229], v[58:61], v232, v232 op_sel_hi:[0,0,0]
	v_mfma_scale_f32_16x16x128_f8f6f4 v[50:53], v[24:31], v[222:229], v[50:53], v232, v232 op_sel_hi:[0,0,0]
	v_mfma_scale_f32_16x16x128_f8f6f4 v[42:45], v[10:17], v[244:251], v[42:45], v232, v232 op_sel_hi:[0,0,0]
	v_mfma_scale_f32_16x16x128_f8f6f4 v[38:41], v[24:31], v[244:251], v[38:41], v232, v232 op_sel_hi:[0,0,0]
	v_mfma_scale_f32_16x16x128_f8f6f4 v[94:97], v[182:189], v[202:209], v[94:97], v232, v232 op_sel_hi:[0,0,0]
	v_mfma_scale_f32_16x16x128_f8f6f4 v[86:89], v[194:201], v[202:209], v[86:89], v232, v232 op_sel_hi:[0,0,0]
	v_mfma_scale_f32_16x16x128_f8f6f4 v[78:81], v[182:189], v[210:217], v[78:81], v232, v232 op_sel_hi:[0,0,0]
	v_mfma_scale_f32_16x16x128_f8f6f4 v[70:73], v[194:201], v[210:217], v[70:73], v232, v232 op_sel_hi:[0,0,0]
	v_mfma_scale_f32_16x16x128_f8f6f4 v[62:65], v[182:189], v[222:229], v[62:65], v232, v232 op_sel_hi:[0,0,0]
	v_mfma_scale_f32_16x16x128_f8f6f4 v[54:57], v[194:201], v[222:229], v[54:57], v232, v232 op_sel_hi:[0,0,0]
	v_mfma_scale_f32_16x16x128_f8f6f4 v[46:49], v[182:189], v[244:251], v[46:49], v232, v232 op_sel_hi:[0,0,0]
	v_mfma_scale_f32_16x16x128_f8f6f4 v[34:37], v[194:201], v[244:251], v[34:37], v232, v232 op_sel_hi:[0,0,0]
	s_setprio 0
	s_barrier
	ds_read_b128 v[10:13], v18
	ds_read_b128 v[14:17], v18 offset:1024
	ds_read_b128 v[24:27], v18 offset:2048
	ds_read_b128 v[28:31], v18 offset:3072
	ds_read_b128 v[182:185], v22
	ds_read_b128 v[186:189], v22 offset:1024
	ds_read_b128 v[194:197], v22 offset:2048
	ds_read_b128 v[198:201], v22 offset:3072
	s_mov_b32 m0, s31
	v_lshl_add_u64 v[20:21], v[178:179], 0, s[52:53]
	ds_read_b128 v[202:205], v191
	ds_read_b128 v[206:209], v191 offset:1024
	ds_read_b128 v[210:213], v191 offset:2048
	ds_read_b128 v[214:217], v191 offset:3072
	ds_read_b128 v[222:225], v191 offset:4096
	ds_read_b128 v[226:229], v191 offset:5120
	ds_read_b128 v[244:247], v191 offset:6144
	ds_read_b128 v[248:251], v191 offset:7168
	global_load_lds_dwordx4 v[20:21], off
	v_lshl_add_u64 v[20:21], v[180:181], 0, s[52:53]
	s_mov_b32 m0, s30
	s_nop 0
	global_load_lds_dwordx4 v[20:21], off
	s_waitcnt vmcnt(8)
	s_waitcnt lgkmcnt(0)
	s_barrier
	s_setprio 1
	s_waitcnt lgkmcnt(0)
	v_mfma_scale_f32_16x16x128_f8f6f4 v[154:157], v[10:17], v[202:209], v[154:157], v232, v232 op_sel_hi:[0,0,0]
	v_mfma_scale_f32_16x16x128_f8f6f4 v[146:149], v[24:31], v[202:209], v[146:149], v232, v232 op_sel_hi:[0,0,0]
	v_mfma_scale_f32_16x16x128_f8f6f4 v[138:141], v[10:17], v[210:217], v[138:141], v232, v232 op_sel_hi:[0,0,0]
	v_mfma_scale_f32_16x16x128_f8f6f4 v[130:133], v[24:31], v[210:217], v[130:133], v232, v232 op_sel_hi:[0,0,0]
	v_mfma_scale_f32_16x16x128_f8f6f4 v[122:125], v[10:17], v[222:229], v[122:125], v232, v232 op_sel_hi:[0,0,0]
	v_mfma_scale_f32_16x16x128_f8f6f4 v[114:117], v[24:31], v[222:229], v[114:117], v232, v232 op_sel_hi:[0,0,0]
	v_mfma_scale_f32_16x16x128_f8f6f4 v[106:109], v[10:17], v[244:251], v[106:109], v232, v232 op_sel_hi:[0,0,0]
	v_mfma_scale_f32_16x16x128_f8f6f4 v[98:101], v[24:31], v[244:251], v[98:101], v232, v232 op_sel_hi:[0,0,0]
	v_mfma_scale_f32_16x16x128_f8f6f4 v[158:161], v[182:189], v[202:209], v[158:161], v232, v232 op_sel_hi:[0,0,0]
	v_mfma_scale_f32_16x16x128_f8f6f4 v[150:153], v[194:201], v[202:209], v[150:153], v232, v232 op_sel_hi:[0,0,0]
	v_mfma_scale_f32_16x16x128_f8f6f4 v[142:145], v[182:189], v[210:217], v[142:145], v232, v232 op_sel_hi:[0,0,0]
	v_mfma_scale_f32_16x16x128_f8f6f4 v[134:137], v[194:201], v[210:217], v[134:137], v232, v232 op_sel_hi:[0,0,0]
	v_mfma_scale_f32_16x16x128_f8f6f4 v[126:129], v[182:189], v[222:229], v[126:129], v232, v232 op_sel_hi:[0,0,0]
	v_mfma_scale_f32_16x16x128_f8f6f4 v[118:121], v[194:201], v[222:229], v[118:121], v232, v232 op_sel_hi:[0,0,0]
	v_mfma_scale_f32_16x16x128_f8f6f4 v[110:113], v[182:189], v[244:251], v[110:113], v232, v232 op_sel_hi:[0,0,0]
	v_mfma_scale_f32_16x16x128_f8f6f4 v[102:105], v[194:201], v[244:251], v[102:105], v232, v232 op_sel_hi:[0,0,0]
	s_setprio 0
	s_barrier
	s_mov_b64 s[52:53], 0x300
	s_mov_b32 m0, s41
	s_add_u32 s2, s28, 0x20300
	v_lshl_add_u64 v[20:21], v[2:3], 0, s[52:53]
	s_addc_u32 s3, s29, 0
	ds_read_b128 v[202:205], v191 offset:16384
	ds_read_b128 v[206:209], v191 offset:17408
	ds_read_b128 v[210:213], v191 offset:18432
	ds_read_b128 v[214:217], v191 offset:19456
	ds_read_b128 v[222:225], v191 offset:20480
	ds_read_b128 v[226:229], v191 offset:21504
	ds_read_b128 v[244:247], v191 offset:22528
	ds_read_b128 v[248:251], v191 offset:23552
	global_load_lds_dwordx4 v[20:21], off
	v_lshl_add_u64 v[20:21], v[4:5], 0, s[52:53]
	s_mov_b32 m0, s42
	v_lshl_add_u64 v[32:33], s[2:3], 0, v[174:175]
	global_load_lds_dwordx4 v[20:21], off
	v_lshl_add_u64 v[20:21], s[2:3], 0, v[164:165]
	s_mov_b32 m0, s44
	v_lshl_add_u64 v[234:235], v[6:7], 0, s[52:53]
	global_load_lds_dwordx4 v[20:21], off
	s_mov_b32 m0, s45
	s_nop 0
	global_load_lds_dwordx4 v[32:33], off
	s_mov_b32 m0, s46
	s_nop 0
	global_load_lds_dwordx4 v[234:235], off
	v_lshl_add_u64 v[234:235], v[8:9], 0, s[52:53]
	s_mov_b32 m0, s47
	s_nop 0
	global_load_lds_dwordx4 v[234:235], off
	s_waitcnt vmcnt(8)
	s_waitcnt lgkmcnt(0)
	s_barrier
	s_setprio 1
	s_waitcnt lgkmcnt(0)
	v_mfma_scale_f32_16x16x128_f8f6f4 v[90:93], v[10:17], v[202:209], v[90:93], v232, v232 op_sel_hi:[0,0,0]
	v_mfma_scale_f32_16x16x128_f8f6f4 v[82:85], v[24:31], v[202:209], v[82:85], v232, v232 op_sel_hi:[0,0,0]
	v_mfma_scale_f32_16x16x128_f8f6f4 v[74:77], v[10:17], v[210:217], v[74:77], v232, v232 op_sel_hi:[0,0,0]
	v_mfma_scale_f32_16x16x128_f8f6f4 v[66:69], v[24:31], v[210:217], v[66:69], v232, v232 op_sel_hi:[0,0,0]
	v_mfma_scale_f32_16x16x128_f8f6f4 v[58:61], v[10:17], v[222:229], v[58:61], v232, v232 op_sel_hi:[0,0,0]
	v_mfma_scale_f32_16x16x128_f8f6f4 v[50:53], v[24:31], v[222:229], v[50:53], v232, v232 op_sel_hi:[0,0,0]
	v_mfma_scale_f32_16x16x128_f8f6f4 v[42:45], v[10:17], v[244:251], v[42:45], v232, v232 op_sel_hi:[0,0,0]
	v_mfma_scale_f32_16x16x128_f8f6f4 v[38:41], v[24:31], v[244:251], v[38:41], v232, v232 op_sel_hi:[0,0,0]
	v_mfma_scale_f32_16x16x128_f8f6f4 v[94:97], v[182:189], v[202:209], v[94:97], v232, v232 op_sel_hi:[0,0,0]
	v_mfma_scale_f32_16x16x128_f8f6f4 v[86:89], v[194:201], v[202:209], v[86:89], v232, v232 op_sel_hi:[0,0,0]
	v_mfma_scale_f32_16x16x128_f8f6f4 v[78:81], v[182:189], v[210:217], v[78:81], v232, v232 op_sel_hi:[0,0,0]
	v_mfma_scale_f32_16x16x128_f8f6f4 v[70:73], v[194:201], v[210:217], v[70:73], v232, v232 op_sel_hi:[0,0,0]
	v_mfma_scale_f32_16x16x128_f8f6f4 v[62:65], v[182:189], v[222:229], v[62:65], v232, v232 op_sel_hi:[0,0,0]
	v_mfma_scale_f32_16x16x128_f8f6f4 v[54:57], v[194:201], v[222:229], v[54:57], v232, v232 op_sel_hi:[0,0,0]
	v_mfma_scale_f32_16x16x128_f8f6f4 v[46:49], v[182:189], v[244:251], v[46:49], v232, v232 op_sel_hi:[0,0,0]
	v_mfma_scale_f32_16x16x128_f8f6f4 v[34:37], v[194:201], v[244:251], v[34:37], v232, v232 op_sel_hi:[0,0,0]
	s_setprio 0
	s_barrier
	ds_read_b128 v[10:13], v192
	ds_read_b128 v[14:17], v192 offset:1024
	ds_read_b128 v[24:27], v192 offset:2048
	ds_read_b128 v[28:31], v192 offset:3072
	ds_read_b128 v[182:185], v193
	ds_read_b128 v[186:189], v193 offset:1024
	ds_read_b128 v[194:197], v193 offset:2048
	ds_read_b128 v[198:201], v193 offset:3072
	s_mov_b32 m0, s48
	v_lshl_add_u64 v[234:235], v[178:179], 0, s[52:53]
	ds_read_b128 v[202:205], v191 offset:32768
	ds_read_b128 v[206:209], v191 offset:33792
	ds_read_b128 v[210:213], v191 offset:34816
	ds_read_b128 v[214:217], v191 offset:35840
	ds_read_b128 v[222:225], v191 offset:36864
	ds_read_b128 v[226:229], v191 offset:37888
	ds_read_b128 v[244:247], v191 offset:38912
	ds_read_b128 v[248:251], v191 offset:39936
	global_load_lds_dwordx4 v[234:235], off
	v_lshl_add_u64 v[234:235], v[180:181], 0, s[52:53]
	s_mov_b32 m0, s49
	s_nop 0
	global_load_lds_dwordx4 v[234:235], off
	s_waitcnt vmcnt(8)
	s_waitcnt lgkmcnt(0)
	s_barrier
	s_setprio 1
	s_waitcnt lgkmcnt(0)
	v_mfma_scale_f32_16x16x128_f8f6f4 v[154:157], v[10:17], v[202:209], v[154:157], v232, v232 op_sel_hi:[0,0,0]
	v_mfma_scale_f32_16x16x128_f8f6f4 v[146:149], v[24:31], v[202:209], v[146:149], v232, v232 op_sel_hi:[0,0,0]
	v_mfma_scale_f32_16x16x128_f8f6f4 v[138:141], v[10:17], v[210:217], v[138:141], v232, v232 op_sel_hi:[0,0,0]
	v_mfma_scale_f32_16x16x128_f8f6f4 v[130:133], v[24:31], v[210:217], v[130:133], v232, v232 op_sel_hi:[0,0,0]
	v_mfma_scale_f32_16x16x128_f8f6f4 v[122:125], v[10:17], v[222:229], v[122:125], v232, v232 op_sel_hi:[0,0,0]
	v_mfma_scale_f32_16x16x128_f8f6f4 v[114:117], v[24:31], v[222:229], v[114:117], v232, v232 op_sel_hi:[0,0,0]
	v_mfma_scale_f32_16x16x128_f8f6f4 v[106:109], v[10:17], v[244:251], v[106:109], v232, v232 op_sel_hi:[0,0,0]
	v_mfma_scale_f32_16x16x128_f8f6f4 v[98:101], v[24:31], v[244:251], v[98:101], v232, v232 op_sel_hi:[0,0,0]
	v_mfma_scale_f32_16x16x128_f8f6f4 v[158:161], v[182:189], v[202:209], v[158:161], v232, v232 op_sel_hi:[0,0,0]
	v_mfma_scale_f32_16x16x128_f8f6f4 v[150:153], v[194:201], v[202:209], v[150:153], v232, v232 op_sel_hi:[0,0,0]
	v_mfma_scale_f32_16x16x128_f8f6f4 v[142:145], v[182:189], v[210:217], v[142:145], v232, v232 op_sel_hi:[0,0,0]
	v_mfma_scale_f32_16x16x128_f8f6f4 v[134:137], v[194:201], v[210:217], v[134:137], v232, v232 op_sel_hi:[0,0,0]
	v_mfma_scale_f32_16x16x128_f8f6f4 v[126:129], v[182:189], v[222:229], v[126:129], v232, v232 op_sel_hi:[0,0,0]
	v_mfma_scale_f32_16x16x128_f8f6f4 v[118:121], v[194:201], v[222:229], v[118:121], v232, v232 op_sel_hi:[0,0,0]
	v_mfma_scale_f32_16x16x128_f8f6f4 v[110:113], v[182:189], v[244:251], v[110:113], v232, v232 op_sel_hi:[0,0,0]
	v_mfma_scale_f32_16x16x128_f8f6f4 v[102:105], v[194:201], v[244:251], v[102:105], v232, v232 op_sel_hi:[0,0,0]
	s_setprio 0
	s_barrier
	s_mov_b64 s[2:3], 0x380
	s_mov_b32 m0, s51
	v_lshl_add_u64 v[2:3], v[2:3], 0, s[2:3]
	ds_read_b128 v[202:205], v191 offset:49152
	ds_read_b128 v[206:209], v191 offset:50176
	ds_read_b128 v[210:213], v191 offset:51200
	ds_read_b128 v[214:217], v191 offset:52224
	ds_read_b128 v[222:225], v191 offset:53248
	ds_read_b128 v[226:229], v191 offset:54272
	ds_read_b128 v[244:247], v191 offset:55296
	ds_read_b128 v[248:251], v191 offset:56320
	global_load_lds_dwordx4 v[2:3], off
	v_lshl_add_u64 v[2:3], v[4:5], 0, s[2:3]
	s_mov_b32 m0, s56
	s_nop 0
	global_load_lds_dwordx4 v[2:3], off
	v_lshl_add_u64 v[2:3], v[20:21], 0, s[72:73]
	s_mov_b32 m0, s62
	s_nop 0
	global_load_lds_dwordx4 v[2:3], off
	v_lshl_add_u64 v[2:3], v[32:33], 0, s[72:73]
	s_mov_b32 m0, s63
	s_nop 0
	global_load_lds_dwordx4 v[2:3], off
	v_lshl_add_u64 v[2:3], v[6:7], 0, s[2:3]
	s_mov_b32 m0, s57
	s_nop 0
	global_load_lds_dwordx4 v[2:3], off
	v_lshl_add_u64 v[2:3], v[8:9], 0, s[2:3]
	s_mov_b32 m0, s60
	s_nop 0
	global_load_lds_dwordx4 v[2:3], off
	s_waitcnt vmcnt(8)
	s_waitcnt lgkmcnt(0)
	s_barrier
	s_setprio 1
	s_waitcnt lgkmcnt(0)
	v_mfma_scale_f32_16x16x128_f8f6f4 v[90:93], v[10:17], v[202:209], v[90:93], v232, v232 op_sel_hi:[0,0,0]
	v_mfma_scale_f32_16x16x128_f8f6f4 v[82:85], v[24:31], v[202:209], v[82:85], v232, v232 op_sel_hi:[0,0,0]
	v_mfma_scale_f32_16x16x128_f8f6f4 v[74:77], v[10:17], v[210:217], v[74:77], v232, v232 op_sel_hi:[0,0,0]
	v_mfma_scale_f32_16x16x128_f8f6f4 v[66:69], v[24:31], v[210:217], v[66:69], v232, v232 op_sel_hi:[0,0,0]
	v_mfma_scale_f32_16x16x128_f8f6f4 v[58:61], v[10:17], v[222:229], v[58:61], v232, v232 op_sel_hi:[0,0,0]
	v_mfma_scale_f32_16x16x128_f8f6f4 v[50:53], v[24:31], v[222:229], v[50:53], v232, v232 op_sel_hi:[0,0,0]
	v_mfma_scale_f32_16x16x128_f8f6f4 v[42:45], v[10:17], v[244:251], v[42:45], v232, v232 op_sel_hi:[0,0,0]
	v_mfma_scale_f32_16x16x128_f8f6f4 v[38:41], v[24:31], v[244:251], v[38:41], v232, v232 op_sel_hi:[0,0,0]
	v_mfma_scale_f32_16x16x128_f8f6f4 v[94:97], v[182:189], v[202:209], v[94:97], v232, v232 op_sel_hi:[0,0,0]
	v_mfma_scale_f32_16x16x128_f8f6f4 v[86:89], v[194:201], v[202:209], v[86:89], v232, v232 op_sel_hi:[0,0,0]
	v_mfma_scale_f32_16x16x128_f8f6f4 v[78:81], v[182:189], v[210:217], v[78:81], v232, v232 op_sel_hi:[0,0,0]
	v_mfma_scale_f32_16x16x128_f8f6f4 v[70:73], v[194:201], v[210:217], v[70:73], v232, v232 op_sel_hi:[0,0,0]
	v_mfma_scale_f32_16x16x128_f8f6f4 v[62:65], v[182:189], v[222:229], v[62:65], v232, v232 op_sel_hi:[0,0,0]
	v_mfma_scale_f32_16x16x128_f8f6f4 v[54:57], v[194:201], v[222:229], v[54:57], v232, v232 op_sel_hi:[0,0,0]
	v_mfma_scale_f32_16x16x128_f8f6f4 v[46:49], v[182:189], v[244:251], v[46:49], v232, v232 op_sel_hi:[0,0,0]
	v_mfma_scale_f32_16x16x128_f8f6f4 v[34:37], v[194:201], v[244:251], v[34:37], v232, v232 op_sel_hi:[0,0,0]
	s_setprio 0
	s_barrier
	ds_read_b128 v[10:13], v18
	ds_read_b128 v[14:17], v18 offset:1024
	ds_read_b128 v[26:29], v18 offset:2048
	ds_read_b128 v[30:33], v18 offset:3072
	ds_read_b128 v[2:5], v22
	ds_read_b128 v[6:9], v22 offset:1024
	ds_read_b128 v[18:21], v22 offset:2048
	ds_read_b128 v[22:25], v22 offset:3072
	s_mov_b32 m0, s31
	v_lshl_add_u64 v[178:179], v[178:179], 0, s[2:3]
	ds_read_b128 v[182:185], v191
	ds_read_b128 v[186:189], v191 offset:1024
	ds_read_b128 v[194:197], v191 offset:2048
	ds_read_b128 v[198:201], v191 offset:3072
	ds_read_b128 v[202:205], v191 offset:4096
	ds_read_b128 v[206:209], v191 offset:5120
	ds_read_b128 v[210:213], v191 offset:6144
	ds_read_b128 v[214:217], v191 offset:7168
	global_load_lds_dwordx4 v[178:179], off
	v_lshl_add_u64 v[178:179], v[180:181], 0, s[2:3]
	s_mov_b32 m0, s30
	s_nop 0
	global_load_lds_dwordx4 v[178:179], off
	s_waitcnt vmcnt(8)
	s_waitcnt lgkmcnt(0)
	s_barrier
	s_setprio 1
	s_waitcnt lgkmcnt(0)
	v_mfma_scale_f32_16x16x128_f8f6f4 v[154:157], v[10:17], v[182:189], v[154:157], v232, v232 op_sel_hi:[0,0,0]
	v_mfma_scale_f32_16x16x128_f8f6f4 v[146:149], v[26:33], v[182:189], v[146:149], v232, v232 op_sel_hi:[0,0,0]
	v_mfma_scale_f32_16x16x128_f8f6f4 v[138:141], v[10:17], v[194:201], v[138:141], v232, v232 op_sel_hi:[0,0,0]
	v_mfma_scale_f32_16x16x128_f8f6f4 v[130:133], v[26:33], v[194:201], v[130:133], v232, v232 op_sel_hi:[0,0,0]
	v_mfma_scale_f32_16x16x128_f8f6f4 v[122:125], v[10:17], v[202:209], v[122:125], v232, v232 op_sel_hi:[0,0,0]
	v_mfma_scale_f32_16x16x128_f8f6f4 v[114:117], v[26:33], v[202:209], v[114:117], v232, v232 op_sel_hi:[0,0,0]
	v_mfma_scale_f32_16x16x128_f8f6f4 v[106:109], v[10:17], v[210:217], v[106:109], v232, v232 op_sel_hi:[0,0,0]
	v_mfma_scale_f32_16x16x128_f8f6f4 v[98:101], v[26:33], v[210:217], v[98:101], v232, v232 op_sel_hi:[0,0,0]
	v_mfma_scale_f32_16x16x128_f8f6f4 v[158:161], v[2:9], v[182:189], v[158:161], v232, v232 op_sel_hi:[0,0,0]
	v_mfma_scale_f32_16x16x128_f8f6f4 v[150:153], v[18:25], v[182:189], v[150:153], v232, v232 op_sel_hi:[0,0,0]
	v_mfma_scale_f32_16x16x128_f8f6f4 v[142:145], v[2:9], v[194:201], v[142:145], v232, v232 op_sel_hi:[0,0,0]
	v_mfma_scale_f32_16x16x128_f8f6f4 v[134:137], v[18:25], v[194:201], v[134:137], v232, v232 op_sel_hi:[0,0,0]
	v_mfma_scale_f32_16x16x128_f8f6f4 v[126:129], v[2:9], v[202:209], v[126:129], v232, v232 op_sel_hi:[0,0,0]
	v_mfma_scale_f32_16x16x128_f8f6f4 v[118:121], v[18:25], v[202:209], v[118:121], v232, v232 op_sel_hi:[0,0,0]
	v_mfma_scale_f32_16x16x128_f8f6f4 v[110:113], v[2:9], v[210:217], v[110:113], v232, v232 op_sel_hi:[0,0,0]
	v_mfma_scale_f32_16x16x128_f8f6f4 v[102:105], v[18:25], v[210:217], v[102:105], v232, v232 op_sel_hi:[0,0,0]
	s_setprio 0
	s_barrier
	s_and_b64 vcc, exec, s[4:5]
	s_mov_b64 s[2:3], 0
	s_cbranch_vccnz .LBB0_1272
	v_mov_b32_e32 v177, s88
	ds_read_b128 v[178:181], v177
	s_waitcnt lgkmcnt(0)
	v_readfirstlane_b32 s58, v178
	v_readfirstlane_b32 s4, v179
	s_cmp_lt_i32 s58, 0
	v_readfirstlane_b32 s5, v180
	s_cbranch_scc1 .LBB0_1272
	s_ashr_i32 s20, s5, 16
	s_and_b32 s91, s5, 0xffff
	s_lshl_b64 s[24:25], s[58:59], 21
	s_add_u32 s5, s34, s24
	s_addc_u32 s23, s35, s25
	s_ashr_i32 s21, s20, 31
	s_lshl_b64 s[24:25], s[20:21], 18
	s_add_u32 s24, s5, s24
	s_addc_u32 s25, s23, s25
	s_lshl_b32 s21, s4, 8
	s_add_u32 s4, s28, 0x20000
	s_addc_u32 s5, s29, 0
	s_branch .LBB0_1273

.LBB0_1282:
	s_mov_b32 m0, s41
	v_lshl_add_u64 v[178:179], s[28:29], 0, v[164:165]
	ds_read_b128 v[194:197], v191 offset:16384
	ds_read_b128 v[198:201], v191 offset:17408
	ds_read_b128 v[202:205], v191 offset:18432
	ds_read_b128 v[206:209], v191 offset:19456
	ds_read_b128 v[210:213], v191 offset:20480
	ds_read_b128 v[214:217], v191 offset:21504
	ds_read_b128 v[222:225], v191 offset:22528
	ds_read_b128 v[226:229], v191 offset:23552
	global_load_lds_dwordx4 v[178:179], off
	v_lshl_add_u64 v[180:181], s[28:29], 0, v[174:175]
	s_mov_b32 m0, s42
	v_lshl_add_u64 v[182:183], s[4:5], 0, v[164:165]
	global_load_lds_dwordx4 v[180:181], off
	s_mov_b32 m0, s44
	v_lshl_add_u64 v[184:185], s[4:5], 0, v[174:175]
	global_load_lds_dwordx4 v[182:183], off
	s_mov_b32 m0, s45
	v_lshl_add_u64 v[186:187], s[6:7], 0, v[168:169]
	global_load_lds_dwordx4 v[184:185], off
	s_mov_b32 m0, s46
	v_lshl_add_u64 v[188:189], s[6:7], 0, v[166:167]
	global_load_lds_dwordx4 v[186:187], off
	s_mov_b32 m0, s47
	s_nop 0
	global_load_lds_dwordx4 v[188:189], off
	s_waitcnt vmcnt(8)
	s_waitcnt lgkmcnt(0)
	s_barrier
	s_setprio 1
	s_waitcnt lgkmcnt(0)
	v_mfma_scale_f32_16x16x128_f8f6f4 v[90:93], v[10:17], v[194:201], v[90:93], v232, v232 op_sel_hi:[0,0,0]
	v_mfma_scale_f32_16x16x128_f8f6f4 v[82:85], v[26:33], v[194:201], v[82:85], v232, v232 op_sel_hi:[0,0,0]
	v_mfma_scale_f32_16x16x128_f8f6f4 v[74:77], v[10:17], v[202:209], v[74:77], v232, v232 op_sel_hi:[0,0,0]
	v_mfma_scale_f32_16x16x128_f8f6f4 v[66:69], v[26:33], v[202:209], v[66:69], v232, v232 op_sel_hi:[0,0,0]
	v_mfma_scale_f32_16x16x128_f8f6f4 v[58:61], v[10:17], v[210:217], v[58:61], v232, v232 op_sel_hi:[0,0,0]
	v_mfma_scale_f32_16x16x128_f8f6f4 v[50:53], v[26:33], v[210:217], v[50:53], v232, v232 op_sel_hi:[0,0,0]
	v_mfma_scale_f32_16x16x128_f8f6f4 v[42:45], v[10:17], v[222:229], v[42:45], v232, v232 op_sel_hi:[0,0,0]
	v_mfma_scale_f32_16x16x128_f8f6f4 v[38:41], v[26:33], v[222:229], v[38:41], v232, v232 op_sel_hi:[0,0,0]
	v_mfma_scale_f32_16x16x128_f8f6f4 v[94:97], v[2:9], v[194:201], v[94:97], v232, v232 op_sel_hi:[0,0,0]
	v_mfma_scale_f32_16x16x128_f8f6f4 v[86:89], v[18:25], v[194:201], v[86:89], v232, v232 op_sel_hi:[0,0,0]
	v_mfma_scale_f32_16x16x128_f8f6f4 v[78:81], v[2:9], v[202:209], v[78:81], v232, v232 op_sel_hi:[0,0,0]
	v_mfma_scale_f32_16x16x128_f8f6f4 v[70:73], v[18:25], v[202:209], v[70:73], v232, v232 op_sel_hi:[0,0,0]
	v_mfma_scale_f32_16x16x128_f8f6f4 v[62:65], v[2:9], v[210:217], v[62:65], v232, v232 op_sel_hi:[0,0,0]
	v_mfma_scale_f32_16x16x128_f8f6f4 v[54:57], v[18:25], v[210:217], v[54:57], v232, v232 op_sel_hi:[0,0,0]
	v_mfma_scale_f32_16x16x128_f8f6f4 v[46:49], v[2:9], v[222:229], v[46:49], v232, v232 op_sel_hi:[0,0,0]
	v_mfma_scale_f32_16x16x128_f8f6f4 v[34:37], v[18:25], v[222:229], v[34:37], v232, v232 op_sel_hi:[0,0,0]
	s_setprio 0
	s_barrier
	ds_read_b128 v[2:5], v192
	ds_read_b128 v[6:9], v192 offset:1024
	ds_read_b128 v[10:13], v192 offset:2048
	ds_read_b128 v[14:17], v192 offset:3072
	ds_read_b128 v[18:21], v193
	ds_read_b128 v[22:25], v193 offset:1024
	ds_read_b128 v[26:29], v193 offset:2048
	ds_read_b128 v[30:33], v193 offset:3072
	s_mov_b32 m0, s48
	v_lshl_add_u64 v[216:217], s[6:7], 0, v[218:219]
	ds_read_b128 v[192:195], v191 offset:32768
	ds_read_b128 v[196:199], v191 offset:33792
	ds_read_b128 v[200:203], v191 offset:34816
	ds_read_b128 v[204:207], v191 offset:35840
	ds_read_b128 v[208:211], v191 offset:36864
	ds_read_b128 v[212:215], v191 offset:37888
	ds_read_b128 v[222:225], v191 offset:38912
	ds_read_b128 v[226:229], v191 offset:39936
	global_load_lds_dwordx4 v[216:217], off
	v_lshl_add_u64 v[216:217], s[6:7], 0, v[172:173]
	s_mov_b32 m0, s49
	s_nop 0
	global_load_lds_dwordx4 v[216:217], off
	s_waitcnt vmcnt(8)
	s_waitcnt lgkmcnt(0)
	s_barrier
	s_setprio 1
	s_waitcnt lgkmcnt(0)
	v_mfma_scale_f32_16x16x128_f8f6f4 v[154:157], v[2:9], v[192:199], v[154:157], v232, v232 op_sel_hi:[0,0,0]
	v_mfma_scale_f32_16x16x128_f8f6f4 v[146:149], v[10:17], v[192:199], v[146:149], v232, v232 op_sel_hi:[0,0,0]
	v_mfma_scale_f32_16x16x128_f8f6f4 v[138:141], v[2:9], v[200:207], v[138:141], v232, v232 op_sel_hi:[0,0,0]
	v_mfma_scale_f32_16x16x128_f8f6f4 v[130:133], v[10:17], v[200:207], v[130:133], v232, v232 op_sel_hi:[0,0,0]
	v_mfma_scale_f32_16x16x128_f8f6f4 v[122:125], v[2:9], v[208:215], v[122:125], v232, v232 op_sel_hi:[0,0,0]
	v_mfma_scale_f32_16x16x128_f8f6f4 v[114:117], v[10:17], v[208:215], v[114:117], v232, v232 op_sel_hi:[0,0,0]
	v_mfma_scale_f32_16x16x128_f8f6f4 v[106:109], v[2:9], v[222:229], v[106:109], v232, v232 op_sel_hi:[0,0,0]
	v_mfma_scale_f32_16x16x128_f8f6f4 v[98:101], v[10:17], v[222:229], v[98:101], v232, v232 op_sel_hi:[0,0,0]
	v_mfma_scale_f32_16x16x128_f8f6f4 v[158:161], v[18:25], v[192:199], v[158:161], v232, v232 op_sel_hi:[0,0,0]
	v_mfma_scale_f32_16x16x128_f8f6f4 v[150:153], v[26:33], v[192:199], v[150:153], v232, v232 op_sel_hi:[0,0,0]
	v_mfma_scale_f32_16x16x128_f8f6f4 v[142:145], v[18:25], v[200:207], v[142:145], v232, v232 op_sel_hi:[0,0,0]
	v_mfma_scale_f32_16x16x128_f8f6f4 v[134:137], v[26:33], v[200:207], v[134:137], v232, v232 op_sel_hi:[0,0,0]
	v_mfma_scale_f32_16x16x128_f8f6f4 v[126:129], v[18:25], v[208:215], v[126:129], v232, v232 op_sel_hi:[0,0,0]
	v_mfma_scale_f32_16x16x128_f8f6f4 v[118:121], v[26:33], v[208:215], v[118:121], v232, v232 op_sel_hi:[0,0,0]
	v_mfma_scale_f32_16x16x128_f8f6f4 v[110:113], v[18:25], v[222:229], v[110:113], v232, v232 op_sel_hi:[0,0,0]
	v_mfma_scale_f32_16x16x128_f8f6f4 v[102:105], v[26:33], v[222:229], v[102:105], v232, v232 op_sel_hi:[0,0,0]
	s_setprio 0
	s_barrier
	s_mov_b32 m0, s51
	v_lshl_add_u64 v[178:179], v[178:179], 0, s[72:73]
	ds_read_b128 v[192:195], v191 offset:49152
	ds_read_b128 v[196:199], v191 offset:50176
	ds_read_b128 v[200:203], v191 offset:51200
	ds_read_b128 v[204:207], v191 offset:52224
	ds_read_b128 v[208:211], v191 offset:53248
	ds_read_b128 v[212:215], v191 offset:54272
	ds_read_b128 v[222:225], v191 offset:55296
	ds_read_b128 v[226:229], v191 offset:56320
	global_load_lds_dwordx4 v[178:179], off
	v_lshl_add_u64 v[178:179], v[180:181], 0, s[72:73]
	s_mov_b32 m0, s56
	s_nop 0
	global_load_lds_dwordx4 v[178:179], off
	v_lshl_add_u64 v[178:179], v[182:183], 0, s[72:73]
	s_mov_b32 m0, s62
	s_nop 0
	global_load_lds_dwordx4 v[178:179], off
	v_lshl_add_u64 v[178:179], v[184:185], 0, s[72:73]
	s_mov_b32 m0, s63
	s_nop 0
	global_load_lds_dwordx4 v[178:179], off
	v_lshl_add_u64 v[178:179], v[186:187], 0, s[72:73]
	s_mov_b32 m0, s57
	s_nop 0
	global_load_lds_dwordx4 v[178:179], off
	v_lshl_add_u64 v[178:179], v[188:189], 0, s[72:73]
	s_mov_b32 m0, s60
	s_nop 0
	global_load_lds_dwordx4 v[178:179], off
	s_waitcnt vmcnt(8)
	s_waitcnt lgkmcnt(0)
	s_barrier
	s_setprio 1
	s_waitcnt lgkmcnt(0)
	v_mfma_scale_f32_16x16x128_f8f6f4 v[90:93], v[2:9], v[192:199], v[90:93], v232, v232 op_sel_hi:[0,0,0]
	v_mfma_scale_f32_16x16x128_f8f6f4 v[82:85], v[10:17], v[192:199], v[82:85], v232, v232 op_sel_hi:[0,0,0]
	v_mfma_scale_f32_16x16x128_f8f6f4 v[74:77], v[2:9], v[200:207], v[74:77], v232, v232 op_sel_hi:[0,0,0]
	v_mfma_scale_f32_16x16x128_f8f6f4 v[66:69], v[10:17], v[200:207], v[66:69], v232, v232 op_sel_hi:[0,0,0]
	v_mfma_scale_f32_16x16x128_f8f6f4 v[58:61], v[2:9], v[208:215], v[58:61], v232, v232 op_sel_hi:[0,0,0]
	v_mfma_scale_f32_16x16x128_f8f6f4 v[50:53], v[10:17], v[208:215], v[50:53], v232, v232 op_sel_hi:[0,0,0]
	v_mfma_scale_f32_16x16x128_f8f6f4 v[42:45], v[2:9], v[222:229], v[42:45], v232, v232 op_sel_hi:[0,0,0]
	v_mfma_scale_f32_16x16x128_f8f6f4 v[38:41], v[10:17], v[222:229], v[38:41], v232, v232 op_sel_hi:[0,0,0]
	v_mfma_scale_f32_16x16x128_f8f6f4 v[94:97], v[18:25], v[192:199], v[94:97], v232, v232 op_sel_hi:[0,0,0]
	v_mfma_scale_f32_16x16x128_f8f6f4 v[86:89], v[26:33], v[192:199], v[86:89], v232, v232 op_sel_hi:[0,0,0]
	v_mfma_scale_f32_16x16x128_f8f6f4 v[78:81], v[18:25], v[200:207], v[78:81], v232, v232 op_sel_hi:[0,0,0]
	v_mfma_scale_f32_16x16x128_f8f6f4 v[70:73], v[26:33], v[200:207], v[70:73], v232, v232 op_sel_hi:[0,0,0]
	v_mfma_scale_f32_16x16x128_f8f6f4 v[62:65], v[18:25], v[208:215], v[62:65], v232, v232 op_sel_hi:[0,0,0]
	v_mfma_scale_f32_16x16x128_f8f6f4 v[54:57], v[26:33], v[208:215], v[54:57], v232, v232 op_sel_hi:[0,0,0]
	v_mfma_scale_f32_16x16x128_f8f6f4 v[46:49], v[18:25], v[222:229], v[46:49], v232, v232 op_sel_hi:[0,0,0]
	v_mfma_scale_f32_16x16x128_f8f6f4 v[34:37], v[26:33], v[222:229], v[34:37], v232, v232 op_sel_hi:[0,0,0]
	s_setprio 0
	s_barrier
	s_andn2_b64 vcc, exec, s[16:17]
	s_cbranch_vccnz .LBB0_1284
	s_barrier

.LBB0_1351:
	s_mov_b32 m0, s47
	ds_read_b128 v[198:201], v197 offset:16384
	ds_read_b128 v[202:205], v197 offset:17408
	ds_read_b128 v[206:209], v197 offset:18432
	ds_read_b128 v[210:213], v197 offset:19456
	ds_read_b128 v[42:45], v197 offset:20480
	ds_read_b128 v[46:49], v197 offset:21504
	ds_read_b128 v[34:37], v197 offset:22528
	ds_read_b128 v[38:41], v197 offset:23552
	global_load_lds_dwordx4 v178, s[88:89]
	s_mov_b32 m0, s48
	v_lshl_add_u64 v[192:193], s[80:81], 0, v[218:219]
	global_load_lds_dwordx4 v182, s[88:89]
	s_mov_b32 m0, s50
	v_lshl_add_u64 v[194:195], s[80:81], 0, v[180:181]
	global_load_lds_dwordx4 v178, s[34:35]
	s_mov_b32 m0, s51
	v_mov_b32_e32 v179, v219
	global_load_lds_dwordx4 v182, s[34:35]
	s_mov_b32 m0, s94
	v_mov_b32_e32 v183, v219
	global_load_lds_dwordx4 v[192:193], off
	s_mov_b32 m0, s95
	v_lshl_add_u64 v[184:185], s[88:89], 0, v[178:179]
	global_load_lds_dwordx4 v[194:195], off
	s_waitcnt vmcnt(8)
	s_waitcnt lgkmcnt(0)
	v_lshl_add_u64 v[186:187], s[88:89], 0, v[182:183]
	v_lshl_add_u64 v[188:189], s[34:35], 0, v[178:179]
	v_lshl_add_u64 v[190:191], s[34:35], 0, v[182:183]
	s_barrier
	s_setprio 1
	s_waitcnt lgkmcnt(0)
	v_mfma_scale_f32_16x16x128_f8f6f4 v[110:113], v[18:25], v[198:205], v[110:113], v232, v232 op_sel_hi:[0,0,0]
	v_mfma_scale_f32_16x16x128_f8f6f4 v[106:109], v[26:33], v[198:205], v[106:109], v232, v232 op_sel_hi:[0,0,0]
	v_mfma_scale_f32_16x16x128_f8f6f4 v[94:97], v[18:25], v[206:213], v[94:97], v232, v232 op_sel_hi:[0,0,0]
	v_mfma_scale_f32_16x16x128_f8f6f4 v[90:93], v[26:33], v[206:213], v[90:93], v232, v232 op_sel_hi:[0,0,0]
	v_mfma_scale_f32_16x16x128_f8f6f4 v[78:81], v[18:25], v[42:49], v[78:81], v232, v232 op_sel_hi:[0,0,0]
	v_mfma_scale_f32_16x16x128_f8f6f4 v[74:77], v[26:33], v[42:49], v[74:77], v232, v232 op_sel_hi:[0,0,0]
	v_mfma_scale_f32_16x16x128_f8f6f4 v[62:65], v[18:25], v[34:41], v[62:65], v232, v232 op_sel_hi:[0,0,0]
	v_mfma_scale_f32_16x16x128_f8f6f4 v[58:61], v[26:33], v[34:41], v[58:61], v232, v232 op_sel_hi:[0,0,0]
	v_mfma_scale_f32_16x16x128_f8f6f4 v[102:105], v[2:9], v[198:205], v[102:105], v232, v232 op_sel_hi:[0,0,0]
	v_mfma_scale_f32_16x16x128_f8f6f4 v[98:101], v[10:17], v[198:205], v[98:101], v232, v232 op_sel_hi:[0,0,0]
	v_mfma_scale_f32_16x16x128_f8f6f4 v[86:89], v[2:9], v[206:213], v[86:89], v232, v232 op_sel_hi:[0,0,0]
	v_mfma_scale_f32_16x16x128_f8f6f4 v[82:85], v[10:17], v[206:213], v[82:85], v232, v232 op_sel_hi:[0,0,0]
	v_mfma_scale_f32_16x16x128_f8f6f4 v[70:73], v[2:9], v[42:49], v[70:73], v232, v232 op_sel_hi:[0,0,0]
	v_mfma_scale_f32_16x16x128_f8f6f4 v[66:69], v[10:17], v[42:49], v[66:69], v232, v232 op_sel_hi:[0,0,0]
	v_mfma_scale_f32_16x16x128_f8f6f4 v[54:57], v[2:9], v[34:41], v[54:57], v232, v232 op_sel_hi:[0,0,0]
	v_mfma_scale_f32_16x16x128_f8f6f4 v[50:53], v[10:17], v[34:41], v[50:53], v232, v232 op_sel_hi:[0,0,0]
	s_setprio 0
	s_barrier
	v_add_u32_e32 v14, s83, v196
	v_add_u32_e32 v30, s55, v196
	ds_read_b128 v[2:5], v14
	ds_read_b128 v[6:9], v14 offset:1024
	ds_read_b128 v[10:13], v14 offset:2048
	ds_read_b128 v[14:17], v14 offset:3072
	ds_read_b128 v[18:21], v30
	ds_read_b128 v[22:25], v30 offset:1024
	ds_read_b128 v[26:29], v30 offset:2048
	ds_read_b128 v[30:33], v30 offset:3072
	s_mov_b32 m0, s38
	v_lshl_add_u64 v[214:215], s[62:63], 0, v[218:219]
	ds_read_b128 v[34:37], v197 offset:32768
	ds_read_b128 v[38:41], v197 offset:33792
	ds_read_b128 v[42:45], v197 offset:34816
	ds_read_b128 v[46:49], v197 offset:35840
	ds_read_b128 v[198:201], v197 offset:36864
	ds_read_b128 v[202:205], v197 offset:37888
	ds_read_b128 v[206:209], v197 offset:38912
	ds_read_b128 v[210:213], v197 offset:39936
	global_load_lds_dwordx4 v[214:215], off
	v_lshl_add_u64 v[214:215], s[62:63], 0, v[180:181]
	s_mov_b32 m0, s66
	s_nop 0
	global_load_lds_dwordx4 v[214:215], off
	s_waitcnt vmcnt(8)
	s_waitcnt lgkmcnt(0)
	s_barrier
	s_setprio 1
	s_waitcnt lgkmcnt(0)
	v_mfma_scale_f32_16x16x128_f8f6f4 v[174:177], v[2:9], v[34:41], v[174:177], v232, v232 op_sel_hi:[0,0,0]
	v_mfma_scale_f32_16x16x128_f8f6f4 v[170:173], v[10:17], v[34:41], v[170:173], v232, v232 op_sel_hi:[0,0,0]
	v_mfma_scale_f32_16x16x128_f8f6f4 v[158:161], v[2:9], v[42:49], v[158:161], v232, v232 op_sel_hi:[0,0,0]
	v_mfma_scale_f32_16x16x128_f8f6f4 v[154:157], v[10:17], v[42:49], v[154:157], v232, v232 op_sel_hi:[0,0,0]
	v_mfma_scale_f32_16x16x128_f8f6f4 v[142:145], v[2:9], v[198:205], v[142:145], v232, v232 op_sel_hi:[0,0,0]
	v_mfma_scale_f32_16x16x128_f8f6f4 v[138:141], v[10:17], v[198:205], v[138:141], v232, v232 op_sel_hi:[0,0,0]
	v_mfma_scale_f32_16x16x128_f8f6f4 v[126:129], v[2:9], v[206:213], v[126:129], v232, v232 op_sel_hi:[0,0,0]
	v_mfma_scale_f32_16x16x128_f8f6f4 v[122:125], v[10:17], v[206:213], v[122:125], v232, v232 op_sel_hi:[0,0,0]
	v_mfma_scale_f32_16x16x128_f8f6f4 v[166:169], v[18:25], v[34:41], v[166:169], v232, v232 op_sel_hi:[0,0,0]
	v_mfma_scale_f32_16x16x128_f8f6f4 v[162:165], v[26:33], v[34:41], v[162:165], v232, v232 op_sel_hi:[0,0,0]
	v_mfma_scale_f32_16x16x128_f8f6f4 v[150:153], v[18:25], v[42:49], v[150:153], v232, v232 op_sel_hi:[0,0,0]
	v_mfma_scale_f32_16x16x128_f8f6f4 v[146:149], v[26:33], v[42:49], v[146:149], v232, v232 op_sel_hi:[0,0,0]
	v_mfma_scale_f32_16x16x128_f8f6f4 v[134:137], v[18:25], v[198:205], v[134:137], v232, v232 op_sel_hi:[0,0,0]
	v_mfma_scale_f32_16x16x128_f8f6f4 v[130:133], v[26:33], v[198:205], v[130:133], v232, v232 op_sel_hi:[0,0,0]
	v_mfma_scale_f32_16x16x128_f8f6f4 v[118:121], v[18:25], v[206:213], v[118:121], v232, v232 op_sel_hi:[0,0,0]
	v_mfma_scale_f32_16x16x128_f8f6f4 v[114:117], v[26:33], v[206:213], v[114:117], v232, v232 op_sel_hi:[0,0,0]
	s_setprio 0
	s_barrier
	s_mov_b32 m0, s52
	v_lshl_add_u64 v[184:185], v[184:185], 0, s[72:73]
	ds_read_b128 v[34:37], v197 offset:49152
	ds_read_b128 v[38:41], v197 offset:50176
	ds_read_b128 v[42:45], v197 offset:51200
	ds_read_b128 v[46:49], v197 offset:52224
	ds_read_b128 v[198:201], v197 offset:53248
	ds_read_b128 v[202:205], v197 offset:54272
	ds_read_b128 v[206:209], v197 offset:55296
	ds_read_b128 v[210:213], v197 offset:56320
	global_load_lds_dwordx4 v[184:185], off
	v_lshl_add_u64 v[184:185], v[186:187], 0, s[72:73]
	s_mov_b32 m0, s82
	s_nop 0
	global_load_lds_dwordx4 v[184:185], off
	v_lshl_add_u64 v[184:185], v[188:189], 0, s[72:73]
	s_mov_b32 m0, s96
	s_nop 0
	global_load_lds_dwordx4 v[184:185], off
	v_lshl_add_u64 v[184:185], v[190:191], 0, s[72:73]
	s_mov_b32 m0, s97
	s_nop 0
	global_load_lds_dwordx4 v[184:185], off
	v_lshl_add_u64 v[184:185], v[192:193], 0, s[72:73]
	s_mov_b32 m0, s53
	s_nop 0
	global_load_lds_dwordx4 v[184:185], off
	v_lshl_add_u64 v[184:185], v[194:195], 0, s[72:73]
	s_mov_b32 m0, s54
	s_nop 0
	global_load_lds_dwordx4 v[184:185], off
	s_waitcnt vmcnt(8)
	s_waitcnt lgkmcnt(0)
	s_barrier
	s_setprio 1
	s_waitcnt lgkmcnt(0)
	v_mfma_scale_f32_16x16x128_f8f6f4 v[110:113], v[2:9], v[34:41], v[110:113], v232, v232 op_sel_hi:[0,0,0]
	v_mfma_scale_f32_16x16x128_f8f6f4 v[106:109], v[10:17], v[34:41], v[106:109], v232, v232 op_sel_hi:[0,0,0]
	v_mfma_scale_f32_16x16x128_f8f6f4 v[94:97], v[2:9], v[42:49], v[94:97], v232, v232 op_sel_hi:[0,0,0]
	v_mfma_scale_f32_16x16x128_f8f6f4 v[90:93], v[10:17], v[42:49], v[90:93], v232, v232 op_sel_hi:[0,0,0]
	v_mfma_scale_f32_16x16x128_f8f6f4 v[78:81], v[2:9], v[198:205], v[78:81], v232, v232 op_sel_hi:[0,0,0]
	v_mfma_scale_f32_16x16x128_f8f6f4 v[74:77], v[10:17], v[198:205], v[74:77], v232, v232 op_sel_hi:[0,0,0]
	v_mfma_scale_f32_16x16x128_f8f6f4 v[62:65], v[2:9], v[206:213], v[62:65], v232, v232 op_sel_hi:[0,0,0]
	v_mfma_scale_f32_16x16x128_f8f6f4 v[58:61], v[10:17], v[206:213], v[58:61], v232, v232 op_sel_hi:[0,0,0]
	v_mfma_scale_f32_16x16x128_f8f6f4 v[102:105], v[18:25], v[34:41], v[102:105], v232, v232 op_sel_hi:[0,0,0]
	v_mfma_scale_f32_16x16x128_f8f6f4 v[98:101], v[26:33], v[34:41], v[98:101], v232, v232 op_sel_hi:[0,0,0]
	v_mfma_scale_f32_16x16x128_f8f6f4 v[86:89], v[18:25], v[42:49], v[86:89], v232, v232 op_sel_hi:[0,0,0]
	v_mfma_scale_f32_16x16x128_f8f6f4 v[82:85], v[26:33], v[42:49], v[82:85], v232, v232 op_sel_hi:[0,0,0]
	v_mfma_scale_f32_16x16x128_f8f6f4 v[70:73], v[18:25], v[198:205], v[70:73], v232, v232 op_sel_hi:[0,0,0]
	v_mfma_scale_f32_16x16x128_f8f6f4 v[66:69], v[26:33], v[198:205], v[66:69], v232, v232 op_sel_hi:[0,0,0]
	v_mfma_scale_f32_16x16x128_f8f6f4 v[54:57], v[18:25], v[206:213], v[54:57], v232, v232 op_sel_hi:[0,0,0]
	v_mfma_scale_f32_16x16x128_f8f6f4 v[50:53], v[26:33], v[206:213], v[50:53], v232, v232 op_sel_hi:[0,0,0]
	s_setprio 0
	s_barrier
	s_add_i32 s93, s93, 2
	s_add_u32 s60, s60, 0x100
	s_addc_u32 s61, s61, 0
	s_cmp_gt_u32 s93, 5
	s_cbranch_scc1 .LBB0_1361
.LBB0_1352:
	s_waitcnt vmcnt(0)
	v_add_u32_e32 v2, s7, v196
	v_add_u32_e32 v14, s49, v196
	ds_read_b128 v[18:21], v2
	ds_read_b128 v[22:25], v2 offset:1024
	ds_read_b128 v[26:29], v2 offset:2048
	ds_read_b128 v[30:33], v2 offset:3072
	ds_read_b128 v[2:5], v14
	ds_read_b128 v[6:9], v14 offset:1024
	ds_read_b128 v[10:13], v14 offset:2048
	ds_read_b128 v[14:17], v14 offset:3072
	s_add_u32 s34, s26, s60
	s_addc_u32 s35, s27, s61
	v_lshl_add_u64 v[192:193], s[34:35], 0, v[218:219]
	v_lshl_add_u64 v[192:193], v[192:193], 0, s[74:75]
	s_add_i32 m0, s94, 0xc000
	v_mov_b32_e32 v181, v219
	ds_read_b128 v[34:37], v197
	ds_read_b128 v[38:41], v197 offset:1024
	ds_read_b128 v[42:45], v197 offset:2048
	ds_read_b128 v[46:49], v197 offset:3072
	ds_read_b128 v[184:187], v197 offset:4096
	ds_read_b128 v[188:191], v197 offset:5120
	ds_read_b128 v[198:201], v197 offset:6144
	ds_read_b128 v[202:205], v197 offset:7168
	global_load_lds_dwordx4 v[192:193], off
	v_lshl_add_u64 v[192:193], s[34:35], 0, v[180:181]
	v_lshl_add_u64 v[192:193], v[192:193], 0, s[74:75]
	s_add_i32 m0, s94, 0xe000
	s_nop 0
	global_load_lds_dwordx4 v[192:193], off
	s_waitcnt vmcnt(8)
	s_waitcnt lgkmcnt(0)
	s_barrier
	s_setprio 1
	s_waitcnt lgkmcnt(0)
	v_mfma_scale_f32_16x16x128_f8f6f4 v[174:177], v[18:25], v[34:41], v[174:177], v232, v232 op_sel_hi:[0,0,0]
	v_mfma_scale_f32_16x16x128_f8f6f4 v[170:173], v[26:33], v[34:41], v[170:173], v232, v232 op_sel_hi:[0,0,0]
	v_mfma_scale_f32_16x16x128_f8f6f4 v[158:161], v[18:25], v[42:49], v[158:161], v232, v232 op_sel_hi:[0,0,0]
	v_mfma_scale_f32_16x16x128_f8f6f4 v[154:157], v[26:33], v[42:49], v[154:157], v232, v232 op_sel_hi:[0,0,0]
	v_mfma_scale_f32_16x16x128_f8f6f4 v[142:145], v[18:25], v[184:191], v[142:145], v232, v232 op_sel_hi:[0,0,0]
	v_mfma_scale_f32_16x16x128_f8f6f4 v[138:141], v[26:33], v[184:191], v[138:141], v232, v232 op_sel_hi:[0,0,0]
	v_mfma_scale_f32_16x16x128_f8f6f4 v[126:129], v[18:25], v[198:205], v[126:129], v232, v232 op_sel_hi:[0,0,0]
	v_mfma_scale_f32_16x16x128_f8f6f4 v[122:125], v[26:33], v[198:205], v[122:125], v232, v232 op_sel_hi:[0,0,0]
	v_mfma_scale_f32_16x16x128_f8f6f4 v[166:169], v[2:9], v[34:41], v[166:169], v232, v232 op_sel_hi:[0,0,0]
	v_mfma_scale_f32_16x16x128_f8f6f4 v[162:165], v[10:17], v[34:41], v[162:165], v232, v232 op_sel_hi:[0,0,0]
	v_mfma_scale_f32_16x16x128_f8f6f4 v[150:153], v[2:9], v[42:49], v[150:153], v232, v232 op_sel_hi:[0,0,0]
	v_mfma_scale_f32_16x16x128_f8f6f4 v[146:149], v[10:17], v[42:49], v[146:149], v232, v232 op_sel_hi:[0,0,0]
	v_mfma_scale_f32_16x16x128_f8f6f4 v[134:137], v[2:9], v[184:191], v[134:137], v232, v232 op_sel_hi:[0,0,0]
	v_mfma_scale_f32_16x16x128_f8f6f4 v[130:133], v[10:17], v[184:191], v[130:133], v232, v232 op_sel_hi:[0,0,0]
	v_mfma_scale_f32_16x16x128_f8f6f4 v[118:121], v[2:9], v[198:205], v[118:121], v232, v232 op_sel_hi:[0,0,0]
	v_mfma_scale_f32_16x16x128_f8f6f4 v[114:117], v[10:17], v[198:205], v[114:117], v232, v232 op_sel_hi:[0,0,0]
	s_cmpk_lg_i32 s60, 0x300
	s_setprio 0
	s_barrier
	s_mov_b64 s[90:91], -1
	s_cbranch_scc0 .LBB0_1354
	s_add_u32 s3, s26, s60
	s_addc_u32 s34, s27, s61
	s_add_u32 s80, s3, 0x100
	s_addc_u32 s81, s34, 0
	s_add_u32 s35, s24, s60
	s_addc_u32 s58, s25, s61
	s_add_u32 s88, s35, 0x100
	s_addc_u32 s89, s58, 0
	s_add_u32 s62, s3, 0x20100
	s_addc_u32 s63, s34, 0
	s_add_u32 s34, s35, 0x20100
	s_addc_u32 s35, s58, 0
	s_mov_b64 s[90:91], 0
